# speedup vs baseline: 1.0035x; 1.0035x over previous
.LE_join19:
	s_waitcnt lgkmcnt(2)
	v_mfma_f32_32x32x16_f16 v[0:15], a[168:171], v[176:179], v[0:15]
	ds_read_b128 v[176:179], v193 offset:28672
	v_mfma_f32_32x32x16_f16 v[16:31], a[168:171], v[180:183], v[16:31]
	ds_read_b128 v[180:183], v193 offset:29696
	v_mfma_f32_32x32x16_f16 v[0:15], a[172:175], v[184:187], v[0:15]
	ds_read_b128 v[184:187], v193 offset:30720
	v_mfma_f32_32x32x16_f16 v[16:31], a[172:175], v[188:191], v[16:31]
	ds_read_b128 v[188:191], v193 offset:31744
	global_load_lds_dwordx4 v192, s[44:45] offset:2048 sc1
	s_waitcnt vmcnt(8)
	s_barrier
	v_mfma_f32_32x32x16_f16 v[0:15], a[176:179], v[160:163], v[0:15]
	ds_read_b128 v[160:163], v193 offset:32768
	v_mfma_f32_32x32x16_f16 v[16:31], a[176:179], v[164:167], v[16:31]
	ds_read_b128 v[164:167], v193 offset:33792
	s_waitcnt lgkmcnt(2)
	v_mfma_f32_32x32x16_f16 v[0:15], a[180:183], v[168:171], v[0:15]
	ds_read_b128 v[168:171], v193 offset:34816
	v_mfma_f32_32x32x16_f16 v[16:31], a[180:183], v[172:175], v[16:31]
	ds_read_b128 v[172:175], v193 offset:35840
	global_load_lds_dwordx4 v192, s[44:45] offset:3072 sc1
	v_mfma_f32_32x32x16_f16 v[0:15], a[184:187], v[176:179], v[0:15]
	ds_read_b128 v[176:179], v193 offset:36864
	v_mfma_f32_32x32x16_f16 v[16:31], a[184:187], v[180:183], v[16:31]
	ds_read_b128 v[180:183], v193 offset:37888
	v_mfma_f32_32x32x16_f16 v[0:15], a[188:191], v[184:187], v[0:15]
	ds_read_b128 v[184:187], v193 offset:38912
	v_mfma_f32_32x32x16_f16 v[16:31], a[188:191], v[188:191], v[16:31]
	ds_read_b128 v[188:191], v193 offset:39936
	s_mov_b32 m0, s54
	s_add_u32 s44, s34, 0x8000
	s_addc_u32 s45, s35, 0
	global_load_lds_dwordx4 v192, s[44:45] sc1
	s_waitcnt lgkmcnt(2)
	v_mfma_f32_32x32x16_f16 v[0:15], a[192:195], v[160:163], v[0:15]
	ds_read_b128 v[160:163], v193 offset:40960
	v_mfma_f32_32x32x16_f16 v[16:31], a[192:195], v[164:167], v[16:31]
	ds_read_b128 v[164:167], v193 offset:41984
	v_mfma_f32_32x32x16_f16 v[0:15], a[196:199], v[168:171], v[0:15]
	ds_read_b128 v[168:171], v193 offset:43008
	v_mfma_f32_32x32x16_f16 v[16:31], a[196:199], v[172:175], v[16:31]
	ds_read_b128 v[172:175], v193 offset:44032
	global_load_lds_dwordx4 v192, s[44:45] offset:1024 sc1
	v_mfma_f32_32x32x16_f16 v[0:15], a[200:203], v[176:179], v[0:15]
	ds_read_b128 v[176:179], v193 offset:45056
	v_mfma_f32_32x32x16_f16 v[16:31], a[200:203], v[180:183], v[16:31]
	ds_read_b128 v[180:183], v193 offset:46080
	s_waitcnt lgkmcnt(2)
	v_mfma_f32_32x32x16_f16 v[0:15], a[204:207], v[184:187], v[0:15]
	ds_read_b128 v[184:187], v193 offset:47104
	s_waitcnt vmcnt(4)
	s_barrier
	v_mov_b32_e32 v199, 4
	s_cmp_eq_u32 s31, 0
	s_cbranch_scc1 .LE_slow20
	global_store_dword v197, v199, s[40:41]
.LE_join21:
	v_mfma_f32_32x32x16_f16 v[16:31], a[204:207], v[188:191], v[16:31]
	ds_read_b128 v[188:191], v193 offset:48128
	global_load_lds_dwordx4 v192, s[44:45] offset:2048 sc1
	v_mfma_f32_32x32x16_f16 v[0:15], a[208:211], v[160:163], v[0:15]
	ds_read_b128 v[160:163], v193 offset:49152
	v_mfma_f32_32x32x16_f16 v[16:31], a[208:211], v[164:167], v[16:31]
	ds_read_b128 v[164:167], v193 offset:50176
	v_mfma_f32_32x32x16_f16 v[0:15], a[212:215], v[168:171], v[0:15]
	ds_read_b128 v[168:171], v193 offset:51200
	s_and_b32 s64, s33, 1
	s_lshl_b32 s64, s64, 22
	s_add_u32 s64, s64, s50
	s_add_u32 s36, s6, s64
	s_addc_u32 s37, s7, 0
	s_lshl_b32 s64, s33, 3
	s_add_u32 s64, s64, s29
	s_lshl_b32 s64, s64, 5
	s_add_u32 s64, s64, s30
	s_lshl_b32 s64, s64, 2
	s_add_u32 s40, s8, s64
	s_addc_u32 s41, s9, 0
	s_lshl_b32 s64, s33, 11
	s_lshl_b32 s65, s29, 8
	s_add_u32 s64, s64, s65
	s_add_u32 s64, s64, 192
	s_lshl_b32 s64, s64, 3
	s_add_u32 s42, s12, s64
	s_addc_u32 s43, s13, 0
	v_mfma_f32_32x32x16_f16 v[16:31], a[212:215], v[172:175], v[16:31]
	ds_read_b128 v[172:175], v193 offset:52224
	global_load_lds_dwordx4 v192, s[44:45] offset:3072 sc1
	s_waitcnt lgkmcnt(2)
	v_mfma_f32_32x32x16_f16 v[0:15], a[216:219], v[176:179], v[0:15]
	ds_read_b128 v[176:179], v193 offset:53248
	v_mfma_f32_32x32x16_f16 v[16:31], a[216:219], v[180:183], v[16:31]
	ds_read_b128 v[180:183], v193 offset:54272
	v_mfma_f32_32x32x16_f16 v[0:15], a[220:223], v[184:187], v[0:15]
	ds_read_b128 v[184:187], v193 offset:55296
	v_mfma_f32_32x32x16_f16 v[16:31], a[220:223], v[188:191], v[16:31]
	ds_read_b128 v[188:191], v193 offset:56320
	s_mov_b32 m0, s55
	s_add_u32 s44, s34, 0x9000
	s_addc_u32 s45, s35, 0
	global_load_lds_dwordx4 v192, s[44:45] sc1
	v_mfma_f32_32x32x16_f16 v[0:15], a[224:227], v[160:163], v[0:15]
	ds_read_b128 v[160:163], v193 offset:57344
	v_mfma_f32_32x32x16_f16 v[16:31], a[224:227], v[164:167], v[16:31]
	ds_read_b128 v[164:167], v193 offset:58368
	s_waitcnt lgkmcnt(2)
	v_mfma_f32_32x32x16_f16 v[0:15], a[228:231], v[168:171], v[0:15]
	ds_read_b128 v[168:171], v193 offset:59392
	v_mfma_f32_32x32x16_f16 v[16:31], a[228:231], v[172:175], v[16:31]
	ds_read_b128 v[172:175], v193 offset:60416
	global_load_lds_dwordx4 v192, s[44:45] offset:1024 sc1
	v_mfma_f32_32x32x16_f16 v[0:15], a[232:235], v[176:179], v[0:15]
	ds_read_b128 v[176:179], v193 offset:61440
	v_mfma_f32_32x32x16_f16 v[16:31], a[232:235], v[180:183], v[16:31]
	ds_read_b128 v[180:183], v193 offset:62464
	v_mfma_f32_32x32x16_f16 v[0:15], a[236:239], v[184:187], v[0:15]
	ds_read_b128 v[184:187], v193 offset:63488
	v_mfma_f32_32x32x16_f16 v[16:31], a[236:239], v[188:191], v[16:31]
	ds_read_b128 v[188:191], v193 offset:64512
	global_load_lds_dwordx4 v192, s[44:45] offset:2048 sc1
	s_waitcnt vmcnt(8)
	s_barrier
	s_waitcnt lgkmcnt(2)
	v_mfma_f32_32x32x16_f16 v[0:15], a[240:243], v[160:163], v[0:15]
	ds_read_b128 v[160:163], v192 offset:0
	v_mfma_f32_32x32x16_f16 v[16:31], a[240:243], v[164:167], v[16:31]
	ds_read_b128 v[164:167], v192 offset:1024
	v_mfma_f32_32x32x16_f16 v[0:15], a[244:247], v[168:171], v[0:15]
	ds_read_b128 v[168:171], v192 offset:2048
	v_mfma_f32_32x32x16_f16 v[16:31], a[244:247], v[172:175], v[16:31]
	ds_read_b128 v[172:175], v192 offset:3072
	global_load_lds_dwordx4 v192, s[44:45] offset:3072 sc1
	v_mfma_f32_32x32x16_f16 v[0:15], a[248:251], v[176:179], v[0:15]
	ds_read_b128 v[176:179], v192 offset:4096
	v_mfma_f32_32x32x16_f16 v[16:31], a[248:251], v[180:183], v[16:31]
	ds_read_b128 v[180:183], v192 offset:5120
	s_waitcnt lgkmcnt(2)
	v_mfma_f32_32x32x16_f16 v[0:15], a[252:255], v[184:187], v[0:15]
	ds_read_b128 v[184:187], v192 offset:6144
	v_mfma_f32_32x32x16_f16 v[16:31], a[252:255], v[188:191], v[16:31]
	ds_read_b128 v[188:191], v192 offset:7168
	s_mov_b32 m0, s56
	s_add_u32 s44, s34, 0x10000
	s_addc_u32 s45, s35, 0
	global_load_lds_dwordx4 v192, s[44:45] sc1
	s_nop 3
	global_load_dword v228, v249, s[42:43] offset:0
	global_load_dword v229, v249, s[42:43] offset:256
	s_waitcnt lgkmcnt(2)
	v_mfma_f32_32x32x16_f16 v[32:47], a[0:3], v[160:163], v[32:47]
	ds_read_b128 v[160:163], v192 offset:8192
	v_exp_f32_e32 v200, v0
	v_mfma_f32_32x32x16_f16 v[48:63], a[0:3], v[164:167], v[48:63]
	ds_read_b128 v[164:167], v192 offset:9216
	s_lshl_b32 s64, s71, 3
	s_add_u32 s64, s64, s29
	s_lshl_b32 s64, s64, 7
	s_add_u32 s38, s8, s64
	s_addc_u32 s39, s9, 0
	global_load_dword v251, v196, s[38:39] sc1
	v_exp_f32_e32 v201, v1
	v_add_f32_e32 v200, 1.0, v200
	v_mfma_f32_32x32x16_f16 v[32:47], a[4:7], v[168:171], v[32:47]
	ds_read_b128 v[168:171], v192 offset:10240
	v_exp_f32_e32 v202, v2
	v_add_f32_e32 v201, 1.0, v201
	v_mfma_f32_32x32x16_f16 v[48:63], a[4:7], v[172:175], v[48:63]
	ds_read_b128 v[172:175], v192 offset:11264
	global_load_lds_dwordx4 v192, s[44:45] offset:1024 sc1
	v_exp_f32_e32 v203, v3
	v_add_f32_e32 v202, 1.0, v202
	v_mfma_f32_32x32x16_f16 v[32:47], a[8:11], v[176:179], v[32:47]
	ds_read_b128 v[176:179], v192 offset:12288
	v_exp_f32_e32 v204, v4
	v_add_f32_e32 v203, 1.0, v203
	v_mfma_f32_32x32x16_f16 v[48:63], a[8:11], v[180:183], v[48:63]
	ds_read_b128 v[180:183], v192 offset:13312
	v_exp_f32_e32 v205, v5
	v_add_f32_e32 v204, 1.0, v204
	s_waitcnt lgkmcnt(2)
	v_mfma_f32_32x32x16_f16 v[32:47], a[12:15], v[184:187], v[32:47]
	ds_read_b128 v[184:187], v192 offset:14336
	v_exp_f32_e32 v206, v6
	v_add_f32_e32 v205, 1.0, v205
	v_mfma_f32_32x32x16_f16 v[48:63], a[12:15], v[188:191], v[48:63]
	ds_read_b128 v[188:191], v192 offset:15360
	global_load_lds_dwordx4 v192, s[44:45] offset:2048 sc1
	v_exp_f32_e32 v207, v7
	v_add_f32_e32 v206, 1.0, v206
	v_mfma_f32_32x32x16_f16 v[32:47], a[16:19], v[160:163], v[32:47]
	ds_read_b128 v[160:163], v192 offset:16384
	v_exp_f32_e32 v208, v8
	v_add_f32_e32 v207, 1.0, v207
	v_mfma_f32_32x32x16_f16 v[48:63], a[16:19], v[164:167], v[48:63]
	ds_read_b128 v[164:167], v192 offset:17408
	v_exp_f32_e32 v209, v9
	v_add_f32_e32 v208, 1.0, v208
	v_mfma_f32_32x32x16_f16 v[32:47], a[20:23], v[168:171], v[32:47]
	ds_read_b128 v[168:171], v192 offset:18432
	v_exp_f32_e32 v210, v10
	v_add_f32_e32 v209, 1.0, v209
	v_mfma_f32_32x32x16_f16 v[48:63], a[20:23], v[172:175], v[48:63]
	ds_read_b128 v[172:175], v192 offset:19456
	global_load_lds_dwordx4 v192, s[44:45] offset:3072 sc1
	v_exp_f32_e32 v211, v11
	v_add_f32_e32 v210, 1.0, v210
	s_waitcnt lgkmcnt(2)
	v_mfma_f32_32x32x16_f16 v[32:47], a[24:27], v[176:179], v[32:47]
	ds_read_b128 v[176:179], v192 offset:20480
	v_exp_f32_e32 v212, v12
	v_add_f32_e32 v211, 1.0, v211
	v_mfma_f32_32x32x16_f16 v[48:63], a[24:27], v[180:183], v[48:63]
	ds_read_b128 v[180:183], v192 offset:21504
	v_exp_f32_e32 v213, v13
	v_add_f32_e32 v212, 1.0, v212
	v_mfma_f32_32x32x16_f16 v[32:47], a[28:31], v[184:187], v[32:47]
	ds_read_b128 v[184:187], v192 offset:22528
	v_exp_f32_e32 v214, v14
	v_add_f32_e32 v213, 1.0, v213
	v_mfma_f32_32x32x16_f16 v[48:63], a[28:31], v[188:191], v[48:63]
	ds_read_b128 v[188:191], v192 offset:23552
	s_mov_b32 m0, s57
	s_add_u32 s44, s34, 0x11000
	s_addc_u32 s45, s35, 0
	global_load_lds_dwordx4 v192, s[44:45] sc1
	v_exp_f32_e32 v215, v15
	v_add_f32_e32 v214, 1.0, v214
	v_mfma_f32_32x32x16_f16 v[32:47], a[32:35], v[160:163], v[32:47]
	ds_read_b128 v[160:163], v192 offset:24576
	v_add_f32_e32 v215, 1.0, v215
	v_rcp_f32_e32 v200, v200
	v_mfma_f32_32x32x16_f16 v[48:63], a[32:35], v[164:167], v[48:63]
	ds_read_b128 v[164:167], v192 offset:25600
	v_rcp_f32_e32 v201, v201
	s_waitcnt lgkmcnt(2)
	v_mfma_f32_32x32x16_f16 v[32:47], a[36:39], v[168:171], v[32:47]
	ds_read_b128 v[168:171], v192 offset:26624
	v_rcp_f32_e32 v202, v202
	v_mfma_f32_32x32x16_f16 v[48:63], a[36:39], v[172:175], v[48:63]
	ds_read_b128 v[172:175], v192 offset:27648
	global_load_lds_dwordx4 v192, s[44:45] offset:1024 sc1
	v_rcp_f32_e32 v203, v203
	v_mfma_f32_32x32x16_f16 v[32:47], a[40:43], v[176:179], v[32:47]
	ds_read_b128 v[176:179], v192 offset:28672
	v_rcp_f32_e32 v204, v204
	v_mfma_f32_32x32x16_f16 v[48:63], a[40:43], v[180:183], v[48:63]
	ds_read_b128 v[180:183], v192 offset:29696
	v_rcp_f32_e32 v205, v205
	v_mul_f32_e32 v204, v204, v128
	v_mfma_f32_32x32x16_f16 v[32:47], a[44:47], v[184:187], v[32:47]
	ds_read_b128 v[184:187], v192 offset:30720
	v_rcp_f32_e32 v206, v206
	v_mul_f32_e32 v205, v205, v129
	v_mfma_f32_32x32x16_f16 v[48:63], a[44:47], v[188:191], v[48:63]
	ds_read_b128 v[188:191], v192 offset:31744
	global_load_lds_dwordx4 v192, s[44:45] offset:2048 sc1
	v_rcp_f32_e32 v207, v207
	v_mul_f32_e32 v206, v206, v130
	s_waitcnt vmcnt(10)
	s_barrier
	s_waitcnt lgkmcnt(2)
	v_mfma_f32_32x32x16_f16 v[32:47], a[48:51], v[160:163], v[32:47]
	ds_read_b128 v[160:163], v192 offset:32768
	v_rcp_f32_e32 v208, v208
	v_mul_f32_e32 v207, v207, v131
	v_mfma_f32_32x32x16_f16 v[48:63], a[48:51], v[164:167], v[48:63]
	ds_read_b128 v[164:167], v192 offset:33792
	v_rcp_f32_e32 v209, v209
	v_fmamk_f32 v208, v208, 0xc0b8aa3b, v198
	v_mfma_f32_32x32x16_f16 v[32:47], a[52:55], v[168:171], v[32:47]
	ds_read_b128 v[168:171], v192 offset:34816
	v_rcp_f32_e32 v210, v210
	v_fmamk_f32 v209, v209, 0xc0b8aa3b, v198
	v_fma_f32 v128, v200, v208, v204
	v_mfma_f32_32x32x16_f16 v[48:63], a[52:55], v[172:175], v[48:63]
	ds_read_b128 v[172:175], v192 offset:35840
	global_load_lds_dwordx4 v192, s[44:45] offset:3072 sc1
	v_rcp_f32_e32 v211, v211
	v_fmamk_f32 v210, v210, 0xc0b8aa3b, v198
	v_fma_f32 v129, v201, v209, v205
	v_mfma_f32_32x32x16_f16 v[32:47], a[56:59], v[176:179], v[32:47]
	ds_read_b128 v[176:179], v192 offset:36864
	v_rcp_f32_e32 v212, v212
	v_fmamk_f32 v211, v211, 0xc0b8aa3b, v198
	v_fma_f32 v130, v202, v210, v206
	v_mfma_f32_32x32x16_f16 v[48:63], a[56:59], v[180:183], v[48:63]
	ds_read_b128 v[180:183], v192 offset:37888
	v_rcp_f32_e32 v213, v213
	v_fma_f32 v131, v203, v211, v207
	s_waitcnt lgkmcnt(2)
	v_mfma_f32_32x32x16_f16 v[32:47], a[60:63], v[184:187], v[32:47]
	ds_read_b128 v[184:187], v192 offset:38912
	v_rcp_f32_e32 v214, v214
	v_mfma_f32_32x32x16_f16 v[48:63], a[60:63], v[188:191], v[48:63]
	ds_read_b128 v[188:191], v192 offset:39936
	s_mov_b32 m0, s58
	s_add_u32 s44, s34, 0x18000
	s_addc_u32 s45, s35, 0
	global_load_lds_dwordx4 v192, s[44:45] sc1
	v_rcp_f32_e32 v215, v215
	v_mfma_f32_32x32x16_f16 v[32:47], a[64:67], v[160:163], v[32:47]
	ds_read_b128 v[160:163], v192 offset:40960
	v_exp_f32_e32 v200, v128
	v_mfma_f32_32x32x16_f16 v[48:63], a[64:67], v[164:167], v[48:63]
	ds_read_b128 v[164:167], v192 offset:41984
	v_exp_f32_e32 v201, v129
	v_add_f32_e32 v200, 1.0, v200
	v_mfma_f32_32x32x16_f16 v[32:47], a[68:71], v[168:171], v[32:47]
	ds_read_b128 v[168:171], v192 offset:43008
	v_exp_f32_e32 v202, v130
	v_add_f32_e32 v201, 1.0, v201
	v_mfma_f32_32x32x16_f16 v[48:63], a[68:71], v[172:175], v[48:63]
	ds_read_b128 v[172:175], v192 offset:44032
	global_load_lds_dwordx4 v192, s[44:45] offset:1024 sc1
	v_exp_f32_e32 v203, v131
	v_add_f32_e32 v202, 1.0, v202
	s_waitcnt lgkmcnt(2)
	v_mfma_f32_32x32x16_f16 v[32:47], a[72:75], v[176:179], v[32:47]
	ds_read_b128 v[176:179], v192 offset:45056
	v_add_f32_e32 v203, 1.0, v203
	v_rcp_f32_e32 v200, v200
	v_mfma_f32_32x32x16_f16 v[48:63], a[72:75], v[180:183], v[48:63]
	ds_read_b128 v[180:183], v192 offset:46080
	v_rcp_f32_e32 v201, v201
	v_fma_f32 v200, v200, 2.0, -1.0
	v_mfma_f32_32x32x16_f16 v[32:47], a[76:79], v[184:187], v[32:47]
	ds_read_b128 v[184:187], v192 offset:47104
	v_rcp_f32_e32 v202, v202
	v_fma_f32 v201, v201, 2.0, -1.0
	v_mul_f32_e32 v216, v212, v200
	v_mfma_f32_32x32x16_f16 v[48:63], a[76:79], v[188:191], v[48:63]
	ds_read_b128 v[188:191], v192 offset:48128
	global_load_lds_dwordx4 v192, s[44:45] offset:2048 sc1
	v_rcp_f32_e32 v203, v203
	v_fma_f32 v202, v202, 2.0, -1.0
	v_mul_f32_e32 v217, v213, v201
	v_mfma_f32_32x32x16_f16 v[32:47], a[80:83], v[160:163], v[32:47]
	ds_read_b128 v[160:163], v192 offset:49152
	v_fma_f32 v203, v203, 2.0, -1.0
	v_mul_f32_e32 v218, v214, v202
	v_exp_f32_e32 v200, v16
	v_mfma_f32_32x32x16_f16 v[48:63], a[80:83], v[164:167], v[48:63]
	ds_read_b128 v[164:167], v192 offset:50176
	v_mul_f32_e32 v219, v215, v203
	v_cvt_pk_f16_f32 v220, v216, v217
	v_exp_f32_e32 v201, v17
	s_waitcnt lgkmcnt(2)
	v_mfma_f32_32x32x16_f16 v[32:47], a[84:87], v[168:171], v[32:47]
	ds_read_b128 v[168:171], v192 offset:51200
	v_cvt_pk_f16_f32 v221, v218, v219
	v_exp_f32_e32 v202, v18
	v_add_f32_e32 v200, 1.0, v200
	v_mfma_f32_32x32x16_f16 v[48:63], a[84:87], v[172:175], v[48:63]
	ds_read_b128 v[172:175], v192 offset:52224
	global_load_lds_dwordx4 v192, s[44:45] offset:3072 sc1
	s_cmp_eq_u32 s33, s60
	s_cbranch_scc1 .LE_ht22

.LE_join29:
	v_mfma_f32_32x32x16_f16 v[48:63], a[168:171], v[180:183], v[48:63]
	ds_read_b128 v[180:183], v193 offset:29696
	v_mfma_f32_32x32x16_f16 v[32:47], a[172:175], v[184:187], v[32:47]
	ds_read_b128 v[184:187], v193 offset:30720
	v_mfma_f32_32x32x16_f16 v[48:63], a[172:175], v[188:191], v[48:63]
	ds_read_b128 v[188:191], v193 offset:31744
	global_load_lds_dwordx4 v192, s[44:45] offset:2048 sc1
	s_waitcnt vmcnt(8)
	s_barrier
	v_mfma_f32_32x32x16_f16 v[32:47], a[176:179], v[160:163], v[32:47]
	ds_read_b128 v[160:163], v193 offset:32768
	v_mfma_f32_32x32x16_f16 v[48:63], a[176:179], v[164:167], v[48:63]
	ds_read_b128 v[164:167], v193 offset:33792
	s_waitcnt lgkmcnt(2)
	v_mfma_f32_32x32x16_f16 v[32:47], a[180:183], v[168:171], v[32:47]
	ds_read_b128 v[168:171], v193 offset:34816
	v_mfma_f32_32x32x16_f16 v[48:63], a[180:183], v[172:175], v[48:63]
	ds_read_b128 v[172:175], v193 offset:35840
	global_load_lds_dwordx4 v192, s[44:45] offset:3072 sc1
	v_mfma_f32_32x32x16_f16 v[32:47], a[184:187], v[176:179], v[32:47]
	ds_read_b128 v[176:179], v193 offset:36864
	v_mfma_f32_32x32x16_f16 v[48:63], a[184:187], v[180:183], v[48:63]
	ds_read_b128 v[180:183], v193 offset:37888
	v_mfma_f32_32x32x16_f16 v[32:47], a[188:191], v[184:187], v[32:47]
	ds_read_b128 v[184:187], v193 offset:38912
	v_mfma_f32_32x32x16_f16 v[48:63], a[188:191], v[188:191], v[48:63]
	ds_read_b128 v[188:191], v193 offset:39936
	s_mov_b32 m0, s54
	s_add_u32 s44, s34, 0x8000
	s_addc_u32 s45, s35, 0
	global_load_lds_dwordx4 v192, s[44:45] sc1
	s_waitcnt lgkmcnt(2)
	v_mfma_f32_32x32x16_f16 v[32:47], a[192:195], v[160:163], v[32:47]
	ds_read_b128 v[160:163], v193 offset:40960
	v_mfma_f32_32x32x16_f16 v[48:63], a[192:195], v[164:167], v[48:63]
	ds_read_b128 v[164:167], v193 offset:41984
	v_mfma_f32_32x32x16_f16 v[32:47], a[196:199], v[168:171], v[32:47]
	ds_read_b128 v[168:171], v193 offset:43008
	v_mfma_f32_32x32x16_f16 v[48:63], a[196:199], v[172:175], v[48:63]
	ds_read_b128 v[172:175], v193 offset:44032
	global_load_lds_dwordx4 v192, s[44:45] offset:1024 sc1
	v_mfma_f32_32x32x16_f16 v[32:47], a[200:203], v[176:179], v[32:47]
	ds_read_b128 v[176:179], v193 offset:45056
	v_mfma_f32_32x32x16_f16 v[48:63], a[200:203], v[180:183], v[48:63]
	ds_read_b128 v[180:183], v193 offset:46080
	s_waitcnt lgkmcnt(2)
	v_mfma_f32_32x32x16_f16 v[32:47], a[204:207], v[184:187], v[32:47]
	ds_read_b128 v[184:187], v193 offset:47104
	v_mfma_f32_32x32x16_f16 v[48:63], a[204:207], v[188:191], v[48:63]
	ds_read_b128 v[188:191], v193 offset:48128
	global_load_lds_dwordx4 v192, s[44:45] offset:2048 sc1
	s_waitcnt vmcnt(5)
	s_barrier
	v_mov_b32_e32 v199, 1
	s_cmp_eq_u32 s31, 0
	s_cbranch_scc1 .LE_slow30
	global_store_dword v197, v199, s[40:41]
.LE_join31:
	v_mfma_f32_32x32x16_f16 v[32:47], a[208:211], v[160:163], v[32:47]
	ds_read_b128 v[160:163], v193 offset:49152
	v_mfma_f32_32x32x16_f16 v[48:63], a[208:211], v[164:167], v[48:63]
	ds_read_b128 v[164:167], v193 offset:50176
	v_mfma_f32_32x32x16_f16 v[32:47], a[212:215], v[168:171], v[32:47]
	ds_read_b128 v[168:171], v193 offset:51200
	v_mfma_f32_32x32x16_f16 v[48:63], a[212:215], v[172:175], v[48:63]
	ds_read_b128 v[172:175], v193 offset:52224
	global_load_lds_dwordx4 v192, s[44:45] offset:3072 sc1
	s_and_b32 s64, s33, 1
	s_lshl_b32 s64, s64, 22
	s_add_u32 s64, s64, s50
	s_add_u32 s64, s64, 0x20000
	s_add_u32 s36, s6, s64
	s_addc_u32 s37, s7, 0
	s_lshl_b32 s64, s33, 3
	s_add_u32 s64, s64, s29
	s_lshl_b32 s64, s64, 5
	s_add_u32 s64, s64, s30
	s_lshl_b32 s64, s64, 2
	s_add_u32 s40, s8, s64
	s_addc_u32 s41, s9, 0
	s_lshl_b32 s64, s61, 11
	s_lshl_b32 s65, s29, 8
	s_add_u32 s64, s64, s65
	s_lshl_b32 s64, s64, 3
	s_add_u32 s42, s12, s64
	s_addc_u32 s43, s13, 0
	s_waitcnt lgkmcnt(2)
	v_mfma_f32_32x32x16_f16 v[32:47], a[216:219], v[176:179], v[32:47]
	ds_read_b128 v[176:179], v193 offset:53248
	v_mfma_f32_32x32x16_f16 v[48:63], a[216:219], v[180:183], v[48:63]
	ds_read_b128 v[180:183], v193 offset:54272
	v_mfma_f32_32x32x16_f16 v[32:47], a[220:223], v[184:187], v[32:47]
	ds_read_b128 v[184:187], v193 offset:55296
	v_mfma_f32_32x32x16_f16 v[48:63], a[220:223], v[188:191], v[48:63]
	ds_read_b128 v[188:191], v193 offset:56320
	s_mov_b32 m0, s55
	s_add_u32 s44, s34, 0x9000
	s_addc_u32 s45, s35, 0
	global_load_lds_dwordx4 v192, s[44:45] sc1
	v_mfma_f32_32x32x16_f16 v[32:47], a[224:227], v[160:163], v[32:47]
	ds_read_b128 v[160:163], v193 offset:57344
	v_mfma_f32_32x32x16_f16 v[48:63], a[224:227], v[164:167], v[48:63]
	ds_read_b128 v[164:167], v193 offset:58368
	s_waitcnt lgkmcnt(2)
	v_mfma_f32_32x32x16_f16 v[32:47], a[228:231], v[168:171], v[32:47]
	ds_read_b128 v[168:171], v193 offset:59392
	v_mfma_f32_32x32x16_f16 v[48:63], a[228:231], v[172:175], v[48:63]
	ds_read_b128 v[172:175], v193 offset:60416
	global_load_lds_dwordx4 v192, s[44:45] offset:1024 sc1
	v_mfma_f32_32x32x16_f16 v[32:47], a[232:235], v[176:179], v[32:47]
	ds_read_b128 v[176:179], v193 offset:61440
	v_mfma_f32_32x32x16_f16 v[48:63], a[232:235], v[180:183], v[48:63]
	ds_read_b128 v[180:183], v193 offset:62464
	v_mfma_f32_32x32x16_f16 v[32:47], a[236:239], v[184:187], v[32:47]
	ds_read_b128 v[184:187], v193 offset:63488
	v_mfma_f32_32x32x16_f16 v[48:63], a[236:239], v[188:191], v[48:63]
	ds_read_b128 v[188:191], v193 offset:64512
	global_load_lds_dwordx4 v192, s[44:45] offset:2048 sc1
	s_waitcnt vmcnt(8)
	s_barrier
	s_waitcnt lgkmcnt(2)
	v_mfma_f32_32x32x16_f16 v[32:47], a[240:243], v[160:163], v[32:47]
	ds_read_b128 v[160:163], v192 offset:0
	v_mfma_f32_32x32x16_f16 v[48:63], a[240:243], v[164:167], v[48:63]
	ds_read_b128 v[164:167], v192 offset:1024
	v_mfma_f32_32x32x16_f16 v[32:47], a[244:247], v[168:171], v[32:47]
	ds_read_b128 v[168:171], v192 offset:2048
	v_mfma_f32_32x32x16_f16 v[48:63], a[244:247], v[172:175], v[48:63]
	ds_read_b128 v[172:175], v192 offset:3072
	global_load_lds_dwordx4 v192, s[44:45] offset:3072 sc1
	v_mfma_f32_32x32x16_f16 v[32:47], a[248:251], v[176:179], v[32:47]
	ds_read_b128 v[176:179], v192 offset:4096
	v_mfma_f32_32x32x16_f16 v[48:63], a[248:251], v[180:183], v[48:63]
	ds_read_b128 v[180:183], v192 offset:5120
	s_waitcnt lgkmcnt(2)
	v_mfma_f32_32x32x16_f16 v[32:47], a[252:255], v[184:187], v[32:47]
	ds_read_b128 v[184:187], v192 offset:6144
	v_mfma_f32_32x32x16_f16 v[48:63], a[252:255], v[188:191], v[48:63]
	ds_read_b128 v[188:191], v192 offset:7168
	s_mov_b32 m0, s56
	s_add_u32 s44, s34, 0x10000
	s_addc_u32 s45, s35, 0
	global_load_lds_dwordx4 v192, s[44:45] sc1
	s_nop 3
	global_load_dword v228, v249, s[42:43] offset:0
	global_load_dword v229, v249, s[42:43] offset:256
	s_waitcnt lgkmcnt(2)
	v_mfma_f32_32x32x16_f16 v[64:79], a[0:3], v[160:163], v[64:79]
	ds_read_b128 v[160:163], v192 offset:8192
	v_exp_f32_e32 v200, v32
	v_mfma_f32_32x32x16_f16 v[80:95], a[0:3], v[164:167], v[80:95]
	ds_read_b128 v[164:167], v192 offset:9216
	s_lshl_b32 s64, s71, 3
	s_add_u32 s64, s64, s29
	s_lshl_b32 s64, s64, 7
	s_add_u32 s38, s8, s64
	s_addc_u32 s39, s9, 0
	global_load_dword v251, v196, s[38:39] sc1
	v_exp_f32_e32 v201, v33
	v_add_f32_e32 v200, 1.0, v200
	v_mfma_f32_32x32x16_f16 v[64:79], a[4:7], v[168:171], v[64:79]
	ds_read_b128 v[168:171], v192 offset:10240
	v_exp_f32_e32 v202, v34
	v_add_f32_e32 v201, 1.0, v201
	v_mfma_f32_32x32x16_f16 v[80:95], a[4:7], v[172:175], v[80:95]
	ds_read_b128 v[172:175], v192 offset:11264
	global_load_lds_dwordx4 v192, s[44:45] offset:1024 sc1
	v_exp_f32_e32 v203, v35
	v_add_f32_e32 v202, 1.0, v202
	v_mfma_f32_32x32x16_f16 v[64:79], a[8:11], v[176:179], v[64:79]
	ds_read_b128 v[176:179], v192 offset:12288
	v_exp_f32_e32 v204, v36
	v_add_f32_e32 v203, 1.0, v203
	v_mfma_f32_32x32x16_f16 v[80:95], a[8:11], v[180:183], v[80:95]
	ds_read_b128 v[180:183], v192 offset:13312
	v_exp_f32_e32 v205, v37
	v_add_f32_e32 v204, 1.0, v204
	s_waitcnt lgkmcnt(2)
	v_mfma_f32_32x32x16_f16 v[64:79], a[12:15], v[184:187], v[64:79]
	ds_read_b128 v[184:187], v192 offset:14336
	v_exp_f32_e32 v206, v38
	v_add_f32_e32 v205, 1.0, v205
	v_mfma_f32_32x32x16_f16 v[80:95], a[12:15], v[188:191], v[80:95]
	ds_read_b128 v[188:191], v192 offset:15360
	global_load_lds_dwordx4 v192, s[44:45] offset:2048 sc1
	v_exp_f32_e32 v207, v39
	v_add_f32_e32 v206, 1.0, v206
	v_mfma_f32_32x32x16_f16 v[64:79], a[16:19], v[160:163], v[64:79]
	ds_read_b128 v[160:163], v192 offset:16384
	v_exp_f32_e32 v208, v40
	v_add_f32_e32 v207, 1.0, v207
	v_mfma_f32_32x32x16_f16 v[80:95], a[16:19], v[164:167], v[80:95]
	ds_read_b128 v[164:167], v192 offset:17408
	v_exp_f32_e32 v209, v41
	v_add_f32_e32 v208, 1.0, v208
	v_mfma_f32_32x32x16_f16 v[64:79], a[20:23], v[168:171], v[64:79]
	ds_read_b128 v[168:171], v192 offset:18432
	v_exp_f32_e32 v210, v42
	v_add_f32_e32 v209, 1.0, v209
	v_mfma_f32_32x32x16_f16 v[80:95], a[20:23], v[172:175], v[80:95]
	ds_read_b128 v[172:175], v192 offset:19456
	global_load_lds_dwordx4 v192, s[44:45] offset:3072 sc1
	v_exp_f32_e32 v211, v43
	v_add_f32_e32 v210, 1.0, v210
	s_waitcnt lgkmcnt(2)
	v_mfma_f32_32x32x16_f16 v[64:79], a[24:27], v[176:179], v[64:79]
	ds_read_b128 v[176:179], v192 offset:20480
	v_exp_f32_e32 v212, v44
	v_add_f32_e32 v211, 1.0, v211
	v_mfma_f32_32x32x16_f16 v[80:95], a[24:27], v[180:183], v[80:95]
	ds_read_b128 v[180:183], v192 offset:21504
	v_exp_f32_e32 v213, v45
	v_add_f32_e32 v212, 1.0, v212
	v_mfma_f32_32x32x16_f16 v[64:79], a[28:31], v[184:187], v[64:79]
	ds_read_b128 v[184:187], v192 offset:22528
	v_exp_f32_e32 v214, v46
	v_add_f32_e32 v213, 1.0, v213
	v_mfma_f32_32x32x16_f16 v[80:95], a[28:31], v[188:191], v[80:95]
	ds_read_b128 v[188:191], v192 offset:23552
	s_mov_b32 m0, s57
	s_add_u32 s44, s34, 0x11000
	s_addc_u32 s45, s35, 0
	global_load_lds_dwordx4 v192, s[44:45] sc1
	v_exp_f32_e32 v215, v47
	v_add_f32_e32 v214, 1.0, v214
	v_mfma_f32_32x32x16_f16 v[64:79], a[32:35], v[160:163], v[64:79]
	ds_read_b128 v[160:163], v192 offset:24576
	v_add_f32_e32 v215, 1.0, v215
	v_rcp_f32_e32 v200, v200
	v_mfma_f32_32x32x16_f16 v[80:95], a[32:35], v[164:167], v[80:95]
	ds_read_b128 v[164:167], v192 offset:25600
	v_rcp_f32_e32 v201, v201
	s_waitcnt lgkmcnt(2)
	v_mfma_f32_32x32x16_f16 v[64:79], a[36:39], v[168:171], v[64:79]
	ds_read_b128 v[168:171], v192 offset:26624
	v_rcp_f32_e32 v202, v202
	v_mfma_f32_32x32x16_f16 v[80:95], a[36:39], v[172:175], v[80:95]
	ds_read_b128 v[172:175], v192 offset:27648
	global_load_lds_dwordx4 v192, s[44:45] offset:1024 sc1
	v_rcp_f32_e32 v203, v203
	v_mfma_f32_32x32x16_f16 v[64:79], a[40:43], v[176:179], v[64:79]
	ds_read_b128 v[176:179], v192 offset:28672
	v_rcp_f32_e32 v204, v204
	v_mfma_f32_32x32x16_f16 v[80:95], a[40:43], v[180:183], v[80:95]
	ds_read_b128 v[180:183], v192 offset:29696
	v_rcp_f32_e32 v205, v205
	v_mul_f32_e32 v204, v204, v136
	v_mfma_f32_32x32x16_f16 v[64:79], a[44:47], v[184:187], v[64:79]
	ds_read_b128 v[184:187], v192 offset:30720
	v_rcp_f32_e32 v206, v206
	v_mul_f32_e32 v205, v205, v137
	v_mfma_f32_32x32x16_f16 v[80:95], a[44:47], v[188:191], v[80:95]
	ds_read_b128 v[188:191], v192 offset:31744
	global_load_lds_dwordx4 v192, s[44:45] offset:2048 sc1
	v_rcp_f32_e32 v207, v207
	v_mul_f32_e32 v206, v206, v138
	s_waitcnt vmcnt(10)
	s_barrier
	s_waitcnt lgkmcnt(2)
	v_mfma_f32_32x32x16_f16 v[64:79], a[48:51], v[160:163], v[64:79]
	ds_read_b128 v[160:163], v192 offset:32768
	v_rcp_f32_e32 v208, v208
	v_mul_f32_e32 v207, v207, v139
	v_mfma_f32_32x32x16_f16 v[80:95], a[48:51], v[164:167], v[80:95]
	ds_read_b128 v[164:167], v192 offset:33792
	v_rcp_f32_e32 v209, v209
	v_fmamk_f32 v208, v208, 0xc0b8aa3b, v198
	v_mfma_f32_32x32x16_f16 v[64:79], a[52:55], v[168:171], v[64:79]
	ds_read_b128 v[168:171], v192 offset:34816
	v_rcp_f32_e32 v210, v210
	v_fmamk_f32 v209, v209, 0xc0b8aa3b, v198
	v_fma_f32 v136, v200, v208, v204
	v_mfma_f32_32x32x16_f16 v[80:95], a[52:55], v[172:175], v[80:95]
	ds_read_b128 v[172:175], v192 offset:35840
	global_load_lds_dwordx4 v192, s[44:45] offset:3072 sc1
	v_rcp_f32_e32 v211, v211
	v_fmamk_f32 v210, v210, 0xc0b8aa3b, v198
	v_fma_f32 v137, v201, v209, v205
	v_mfma_f32_32x32x16_f16 v[64:79], a[56:59], v[176:179], v[64:79]
	ds_read_b128 v[176:179], v192 offset:36864
	v_rcp_f32_e32 v212, v212
	v_fmamk_f32 v211, v211, 0xc0b8aa3b, v198
	v_fma_f32 v138, v202, v210, v206
	v_mfma_f32_32x32x16_f16 v[80:95], a[56:59], v[180:183], v[80:95]
	ds_read_b128 v[180:183], v192 offset:37888
	v_rcp_f32_e32 v213, v213
	v_fma_f32 v139, v203, v211, v207
	s_waitcnt lgkmcnt(2)
	v_mfma_f32_32x32x16_f16 v[64:79], a[60:63], v[184:187], v[64:79]
	ds_read_b128 v[184:187], v192 offset:38912
	v_rcp_f32_e32 v214, v214
	v_mfma_f32_32x32x16_f16 v[80:95], a[60:63], v[188:191], v[80:95]
	ds_read_b128 v[188:191], v192 offset:39936
	s_mov_b32 m0, s58
	s_add_u32 s44, s34, 0x18000
	s_addc_u32 s45, s35, 0
	global_load_lds_dwordx4 v192, s[44:45] sc1
	v_rcp_f32_e32 v215, v215
	v_mfma_f32_32x32x16_f16 v[64:79], a[64:67], v[160:163], v[64:79]
	ds_read_b128 v[160:163], v192 offset:40960
	v_exp_f32_e32 v200, v136
	v_mfma_f32_32x32x16_f16 v[80:95], a[64:67], v[164:167], v[80:95]
	ds_read_b128 v[164:167], v192 offset:41984
	v_exp_f32_e32 v201, v137
	v_add_f32_e32 v200, 1.0, v200
	v_mfma_f32_32x32x16_f16 v[64:79], a[68:71], v[168:171], v[64:79]
	ds_read_b128 v[168:171], v192 offset:43008
	v_exp_f32_e32 v202, v138
	v_add_f32_e32 v201, 1.0, v201
	v_mfma_f32_32x32x16_f16 v[80:95], a[68:71], v[172:175], v[80:95]
	ds_read_b128 v[172:175], v192 offset:44032
	global_load_lds_dwordx4 v192, s[44:45] offset:1024 sc1
	v_exp_f32_e32 v203, v139
	v_add_f32_e32 v202, 1.0, v202
	s_waitcnt lgkmcnt(2)
	v_mfma_f32_32x32x16_f16 v[64:79], a[72:75], v[176:179], v[64:79]
	ds_read_b128 v[176:179], v192 offset:45056
	v_add_f32_e32 v203, 1.0, v203
	v_rcp_f32_e32 v200, v200
	v_mfma_f32_32x32x16_f16 v[80:95], a[72:75], v[180:183], v[80:95]
	ds_read_b128 v[180:183], v192 offset:46080
	v_rcp_f32_e32 v201, v201
	v_fma_f32 v200, v200, 2.0, -1.0
	v_mfma_f32_32x32x16_f16 v[64:79], a[76:79], v[184:187], v[64:79]
	ds_read_b128 v[184:187], v192 offset:47104
	v_rcp_f32_e32 v202, v202
	v_fma_f32 v201, v201, 2.0, -1.0
	v_mul_f32_e32 v216, v212, v200
	v_mfma_f32_32x32x16_f16 v[80:95], a[76:79], v[188:191], v[80:95]
	ds_read_b128 v[188:191], v192 offset:48128
	global_load_lds_dwordx4 v192, s[44:45] offset:2048 sc1
	v_rcp_f32_e32 v203, v203
	v_fma_f32 v202, v202, 2.0, -1.0
	v_mul_f32_e32 v217, v213, v201
	v_mfma_f32_32x32x16_f16 v[64:79], a[80:83], v[160:163], v[64:79]
	ds_read_b128 v[160:163], v192 offset:49152
	v_fma_f32 v203, v203, 2.0, -1.0
	v_mul_f32_e32 v218, v214, v202
	v_exp_f32_e32 v200, v48
	v_mfma_f32_32x32x16_f16 v[80:95], a[80:83], v[164:167], v[80:95]
	ds_read_b128 v[164:167], v192 offset:50176
	v_mul_f32_e32 v219, v215, v203
	v_cvt_pk_f16_f32 v220, v216, v217
	v_exp_f32_e32 v201, v49
	s_waitcnt lgkmcnt(2)
	v_mfma_f32_32x32x16_f16 v[64:79], a[84:87], v[168:171], v[64:79]
	ds_read_b128 v[168:171], v192 offset:51200
	v_cvt_pk_f16_f32 v221, v218, v219
	v_exp_f32_e32 v202, v50
	v_add_f32_e32 v200, 1.0, v200
	v_mfma_f32_32x32x16_f16 v[80:95], a[84:87], v[172:175], v[80:95]
	ds_read_b128 v[172:175], v192 offset:52224
	global_load_lds_dwordx4 v192, s[44:45] offset:3072 sc1
	s_cmp_eq_u32 s33, s60
	s_cbranch_scc1 .LE_ht32

.LE_join39:
	v_mfma_f32_32x32x16_f16 v[80:95], a[168:171], v[180:183], v[80:95]
	ds_read_b128 v[180:183], v193 offset:29696
	v_mfma_f32_32x32x16_f16 v[64:79], a[172:175], v[184:187], v[64:79]
	ds_read_b128 v[184:187], v193 offset:30720
	v_mfma_f32_32x32x16_f16 v[80:95], a[172:175], v[188:191], v[80:95]
	ds_read_b128 v[188:191], v193 offset:31744
	global_load_lds_dwordx4 v192, s[44:45] offset:2048 sc1
	s_waitcnt vmcnt(8)
	s_barrier
	v_mfma_f32_32x32x16_f16 v[64:79], a[176:179], v[160:163], v[64:79]
	ds_read_b128 v[160:163], v193 offset:32768
	v_mfma_f32_32x32x16_f16 v[80:95], a[176:179], v[164:167], v[80:95]
	ds_read_b128 v[164:167], v193 offset:33792
	s_waitcnt lgkmcnt(2)
	v_mfma_f32_32x32x16_f16 v[64:79], a[180:183], v[168:171], v[64:79]
	ds_read_b128 v[168:171], v193 offset:34816
	v_mfma_f32_32x32x16_f16 v[80:95], a[180:183], v[172:175], v[80:95]
	ds_read_b128 v[172:175], v193 offset:35840
	global_load_lds_dwordx4 v192, s[44:45] offset:3072 sc1
	v_mfma_f32_32x32x16_f16 v[64:79], a[184:187], v[176:179], v[64:79]
	ds_read_b128 v[176:179], v193 offset:36864
	v_mfma_f32_32x32x16_f16 v[80:95], a[184:187], v[180:183], v[80:95]
	ds_read_b128 v[180:183], v193 offset:37888
	v_mfma_f32_32x32x16_f16 v[64:79], a[188:191], v[184:187], v[64:79]
	ds_read_b128 v[184:187], v193 offset:38912
	v_mfma_f32_32x32x16_f16 v[80:95], a[188:191], v[188:191], v[80:95]
	ds_read_b128 v[188:191], v193 offset:39936
	s_mov_b32 m0, s54
	s_add_u32 s44, s34, 0x8000
	s_addc_u32 s45, s35, 0
	global_load_lds_dwordx4 v192, s[44:45] sc1
	s_waitcnt lgkmcnt(2)
	v_mfma_f32_32x32x16_f16 v[64:79], a[192:195], v[160:163], v[64:79]
	ds_read_b128 v[160:163], v193 offset:40960
	v_mfma_f32_32x32x16_f16 v[80:95], a[192:195], v[164:167], v[80:95]
	ds_read_b128 v[164:167], v193 offset:41984
	v_mfma_f32_32x32x16_f16 v[64:79], a[196:199], v[168:171], v[64:79]
	ds_read_b128 v[168:171], v193 offset:43008
	v_mfma_f32_32x32x16_f16 v[80:95], a[196:199], v[172:175], v[80:95]
	ds_read_b128 v[172:175], v193 offset:44032
	global_load_lds_dwordx4 v192, s[44:45] offset:1024 sc1
	v_mfma_f32_32x32x16_f16 v[64:79], a[200:203], v[176:179], v[64:79]
	ds_read_b128 v[176:179], v193 offset:45056
	v_mfma_f32_32x32x16_f16 v[80:95], a[200:203], v[180:183], v[80:95]
	ds_read_b128 v[180:183], v193 offset:46080
	s_waitcnt lgkmcnt(2)
	v_mfma_f32_32x32x16_f16 v[64:79], a[204:207], v[184:187], v[64:79]
	ds_read_b128 v[184:187], v193 offset:47104
	v_mfma_f32_32x32x16_f16 v[80:95], a[204:207], v[188:191], v[80:95]
	ds_read_b128 v[188:191], v193 offset:48128
	global_load_lds_dwordx4 v192, s[44:45] offset:2048 sc1
	s_waitcnt vmcnt(5)
	s_barrier
	v_mov_b32_e32 v199, 2
	s_cmp_eq_u32 s31, 0
	s_cbranch_scc1 .LE_slow40
	global_store_dword v197, v199, s[40:41]
.LE_join41:
	v_mfma_f32_32x32x16_f16 v[64:79], a[208:211], v[160:163], v[64:79]
	ds_read_b128 v[160:163], v193 offset:49152
	v_mfma_f32_32x32x16_f16 v[80:95], a[208:211], v[164:167], v[80:95]
	ds_read_b128 v[164:167], v193 offset:50176
	v_mfma_f32_32x32x16_f16 v[64:79], a[212:215], v[168:171], v[64:79]
	ds_read_b128 v[168:171], v193 offset:51200
	v_mfma_f32_32x32x16_f16 v[80:95], a[212:215], v[172:175], v[80:95]
	ds_read_b128 v[172:175], v193 offset:52224
	global_load_lds_dwordx4 v192, s[44:45] offset:3072 sc1
	s_and_b32 s64, s33, 1
	s_lshl_b32 s64, s64, 22
	s_add_u32 s64, s64, s50
	s_add_u32 s64, s64, 0x40000
	s_add_u32 s36, s6, s64
	s_addc_u32 s37, s7, 0
	s_lshl_b32 s64, s33, 3
	s_add_u32 s64, s64, s29
	s_lshl_b32 s64, s64, 5
	s_add_u32 s64, s64, s30
	s_lshl_b32 s64, s64, 2
	s_add_u32 s40, s8, s64
	s_addc_u32 s41, s9, 0
	s_lshl_b32 s64, s61, 11
	s_lshl_b32 s65, s29, 8
	s_add_u32 s64, s64, s65
	s_add_u32 s64, s64, 64
	s_lshl_b32 s64, s64, 3
	s_add_u32 s42, s12, s64
	s_addc_u32 s43, s13, 0
	s_waitcnt lgkmcnt(2)
	v_mfma_f32_32x32x16_f16 v[64:79], a[216:219], v[176:179], v[64:79]
	ds_read_b128 v[176:179], v193 offset:53248
	v_mfma_f32_32x32x16_f16 v[80:95], a[216:219], v[180:183], v[80:95]
	ds_read_b128 v[180:183], v193 offset:54272
	v_mfma_f32_32x32x16_f16 v[64:79], a[220:223], v[184:187], v[64:79]
	ds_read_b128 v[184:187], v193 offset:55296
	v_mfma_f32_32x32x16_f16 v[80:95], a[220:223], v[188:191], v[80:95]
	ds_read_b128 v[188:191], v193 offset:56320
	s_mov_b32 m0, s55
	s_add_u32 s44, s34, 0x9000
	s_addc_u32 s45, s35, 0
	global_load_lds_dwordx4 v192, s[44:45] sc1
	v_mfma_f32_32x32x16_f16 v[64:79], a[224:227], v[160:163], v[64:79]
	ds_read_b128 v[160:163], v193 offset:57344
	v_mfma_f32_32x32x16_f16 v[80:95], a[224:227], v[164:167], v[80:95]
	ds_read_b128 v[164:167], v193 offset:58368
	s_waitcnt lgkmcnt(2)
	v_mfma_f32_32x32x16_f16 v[64:79], a[228:231], v[168:171], v[64:79]
	ds_read_b128 v[168:171], v193 offset:59392
	v_mfma_f32_32x32x16_f16 v[80:95], a[228:231], v[172:175], v[80:95]
	ds_read_b128 v[172:175], v193 offset:60416
	global_load_lds_dwordx4 v192, s[44:45] offset:1024 sc1
	v_mfma_f32_32x32x16_f16 v[64:79], a[232:235], v[176:179], v[64:79]
	ds_read_b128 v[176:179], v193 offset:61440
	v_mfma_f32_32x32x16_f16 v[80:95], a[232:235], v[180:183], v[80:95]
	ds_read_b128 v[180:183], v193 offset:62464
	v_mfma_f32_32x32x16_f16 v[64:79], a[236:239], v[184:187], v[64:79]
	ds_read_b128 v[184:187], v193 offset:63488
	v_mfma_f32_32x32x16_f16 v[80:95], a[236:239], v[188:191], v[80:95]
	ds_read_b128 v[188:191], v193 offset:64512
	global_load_lds_dwordx4 v192, s[44:45] offset:2048 sc1
	s_waitcnt vmcnt(8)
	s_barrier
	s_waitcnt lgkmcnt(2)
	v_mfma_f32_32x32x16_f16 v[64:79], a[240:243], v[160:163], v[64:79]
	ds_read_b128 v[160:163], v192 offset:0
	v_mfma_f32_32x32x16_f16 v[80:95], a[240:243], v[164:167], v[80:95]
	ds_read_b128 v[164:167], v192 offset:1024
	v_mfma_f32_32x32x16_f16 v[64:79], a[244:247], v[168:171], v[64:79]
	ds_read_b128 v[168:171], v192 offset:2048
	v_mfma_f32_32x32x16_f16 v[80:95], a[244:247], v[172:175], v[80:95]
	ds_read_b128 v[172:175], v192 offset:3072
	global_load_lds_dwordx4 v192, s[44:45] offset:3072 sc1
	v_mfma_f32_32x32x16_f16 v[64:79], a[248:251], v[176:179], v[64:79]
	ds_read_b128 v[176:179], v192 offset:4096
	v_mfma_f32_32x32x16_f16 v[80:95], a[248:251], v[180:183], v[80:95]
	ds_read_b128 v[180:183], v192 offset:5120
	s_waitcnt lgkmcnt(2)
	v_mfma_f32_32x32x16_f16 v[64:79], a[252:255], v[184:187], v[64:79]
	ds_read_b128 v[184:187], v192 offset:6144
	v_mfma_f32_32x32x16_f16 v[80:95], a[252:255], v[188:191], v[80:95]
	ds_read_b128 v[188:191], v192 offset:7168
	s_mov_b32 m0, s56
	s_add_u32 s44, s34, 0x10000
	s_addc_u32 s45, s35, 0
	global_load_lds_dwordx4 v192, s[44:45] sc1
	s_nop 3
	global_load_dword v228, v249, s[42:43] offset:0
	global_load_dword v229, v249, s[42:43] offset:256
	s_waitcnt lgkmcnt(2)
	v_mfma_f32_32x32x16_f16 v[96:111], a[0:3], v[160:163], v[96:111]
	ds_read_b128 v[160:163], v192 offset:8192
	v_exp_f32_e32 v200, v64
	v_mfma_f32_32x32x16_f16 v[112:127], a[0:3], v[164:167], v[112:127]
	ds_read_b128 v[164:167], v192 offset:9216
	s_lshl_b32 s64, s33, 3
	s_add_u32 s64, s64, s29
	s_lshl_b32 s64, s64, 7
	s_add_u32 s38, s8, s64
	s_addc_u32 s39, s9, 0
	global_load_dword v251, v196, s[38:39] sc1
	v_exp_f32_e32 v201, v65
	v_add_f32_e32 v200, 1.0, v200
	v_mfma_f32_32x32x16_f16 v[96:111], a[4:7], v[168:171], v[96:111]
	ds_read_b128 v[168:171], v192 offset:10240
	v_exp_f32_e32 v202, v66
	v_add_f32_e32 v201, 1.0, v201
	v_mfma_f32_32x32x16_f16 v[112:127], a[4:7], v[172:175], v[112:127]
	ds_read_b128 v[172:175], v192 offset:11264
	global_load_lds_dwordx4 v192, s[44:45] offset:1024 sc1
	v_exp_f32_e32 v203, v67
	v_add_f32_e32 v202, 1.0, v202
	v_mfma_f32_32x32x16_f16 v[96:111], a[8:11], v[176:179], v[96:111]
	ds_read_b128 v[176:179], v192 offset:12288
	v_exp_f32_e32 v204, v68
	v_add_f32_e32 v203, 1.0, v203
	v_mfma_f32_32x32x16_f16 v[112:127], a[8:11], v[180:183], v[112:127]
	ds_read_b128 v[180:183], v192 offset:13312
	v_exp_f32_e32 v205, v69
	v_add_f32_e32 v204, 1.0, v204
	s_waitcnt lgkmcnt(2)
	v_mfma_f32_32x32x16_f16 v[96:111], a[12:15], v[184:187], v[96:111]
	ds_read_b128 v[184:187], v192 offset:14336
	v_exp_f32_e32 v206, v70
	v_add_f32_e32 v205, 1.0, v205
	v_mfma_f32_32x32x16_f16 v[112:127], a[12:15], v[188:191], v[112:127]
	ds_read_b128 v[188:191], v192 offset:15360
	global_load_lds_dwordx4 v192, s[44:45] offset:2048 sc1
	v_exp_f32_e32 v207, v71
	v_add_f32_e32 v206, 1.0, v206
	v_mfma_f32_32x32x16_f16 v[96:111], a[16:19], v[160:163], v[96:111]
	ds_read_b128 v[160:163], v192 offset:16384
	v_exp_f32_e32 v208, v72
	v_add_f32_e32 v207, 1.0, v207
	v_mfma_f32_32x32x16_f16 v[112:127], a[16:19], v[164:167], v[112:127]
	ds_read_b128 v[164:167], v192 offset:17408
	v_exp_f32_e32 v209, v73
	v_add_f32_e32 v208, 1.0, v208
	v_mfma_f32_32x32x16_f16 v[96:111], a[20:23], v[168:171], v[96:111]
	ds_read_b128 v[168:171], v192 offset:18432
	v_exp_f32_e32 v210, v74
	v_add_f32_e32 v209, 1.0, v209
	v_mfma_f32_32x32x16_f16 v[112:127], a[20:23], v[172:175], v[112:127]
	ds_read_b128 v[172:175], v192 offset:19456
	global_load_lds_dwordx4 v192, s[44:45] offset:3072 sc1
	v_exp_f32_e32 v211, v75
	v_add_f32_e32 v210, 1.0, v210
	s_waitcnt lgkmcnt(2)
	v_mfma_f32_32x32x16_f16 v[96:111], a[24:27], v[176:179], v[96:111]
	ds_read_b128 v[176:179], v192 offset:20480
	v_exp_f32_e32 v212, v76
	v_add_f32_e32 v211, 1.0, v211
	v_mfma_f32_32x32x16_f16 v[112:127], a[24:27], v[180:183], v[112:127]
	ds_read_b128 v[180:183], v192 offset:21504
	v_exp_f32_e32 v213, v77
	v_add_f32_e32 v212, 1.0, v212
	v_mfma_f32_32x32x16_f16 v[96:111], a[28:31], v[184:187], v[96:111]
	ds_read_b128 v[184:187], v192 offset:22528
	v_exp_f32_e32 v214, v78
	v_add_f32_e32 v213, 1.0, v213
	v_mfma_f32_32x32x16_f16 v[112:127], a[28:31], v[188:191], v[112:127]
	ds_read_b128 v[188:191], v192 offset:23552
	s_mov_b32 m0, s57
	s_add_u32 s44, s34, 0x11000
	s_addc_u32 s45, s35, 0
	global_load_lds_dwordx4 v192, s[44:45] sc1
	v_exp_f32_e32 v215, v79
	v_add_f32_e32 v214, 1.0, v214
	v_mfma_f32_32x32x16_f16 v[96:111], a[32:35], v[160:163], v[96:111]
	ds_read_b128 v[160:163], v192 offset:24576
	v_add_f32_e32 v215, 1.0, v215
	v_rcp_f32_e32 v200, v200
	v_mfma_f32_32x32x16_f16 v[112:127], a[32:35], v[164:167], v[112:127]
	ds_read_b128 v[164:167], v192 offset:25600
	v_rcp_f32_e32 v201, v201
	s_waitcnt lgkmcnt(2)
	v_mfma_f32_32x32x16_f16 v[96:111], a[36:39], v[168:171], v[96:111]
	ds_read_b128 v[168:171], v192 offset:26624
	v_rcp_f32_e32 v202, v202
	v_mfma_f32_32x32x16_f16 v[112:127], a[36:39], v[172:175], v[112:127]
	ds_read_b128 v[172:175], v192 offset:27648
	global_load_lds_dwordx4 v192, s[44:45] offset:1024 sc1
	v_rcp_f32_e32 v203, v203
	v_mfma_f32_32x32x16_f16 v[96:111], a[40:43], v[176:179], v[96:111]
	ds_read_b128 v[176:179], v192 offset:28672
	v_rcp_f32_e32 v204, v204
	v_mfma_f32_32x32x16_f16 v[112:127], a[40:43], v[180:183], v[112:127]
	ds_read_b128 v[180:183], v192 offset:29696
	v_rcp_f32_e32 v205, v205
	v_mul_f32_e32 v204, v204, v144
	v_mfma_f32_32x32x16_f16 v[96:111], a[44:47], v[184:187], v[96:111]
	ds_read_b128 v[184:187], v192 offset:30720
	v_rcp_f32_e32 v206, v206
	v_mul_f32_e32 v205, v205, v145
	v_mfma_f32_32x32x16_f16 v[112:127], a[44:47], v[188:191], v[112:127]
	ds_read_b128 v[188:191], v192 offset:31744
	global_load_lds_dwordx4 v192, s[44:45] offset:2048 sc1
	v_rcp_f32_e32 v207, v207
	v_mul_f32_e32 v206, v206, v146
	s_waitcnt vmcnt(10)
	s_barrier
	s_waitcnt lgkmcnt(2)
	v_mfma_f32_32x32x16_f16 v[96:111], a[48:51], v[160:163], v[96:111]
	ds_read_b128 v[160:163], v192 offset:32768
	v_rcp_f32_e32 v208, v208
	v_mul_f32_e32 v207, v207, v147
	v_mfma_f32_32x32x16_f16 v[112:127], a[48:51], v[164:167], v[112:127]
	ds_read_b128 v[164:167], v192 offset:33792
	v_rcp_f32_e32 v209, v209
	v_fmamk_f32 v208, v208, 0xc0b8aa3b, v198
	v_mfma_f32_32x32x16_f16 v[96:111], a[52:55], v[168:171], v[96:111]
	ds_read_b128 v[168:171], v192 offset:34816
	v_rcp_f32_e32 v210, v210
	v_fmamk_f32 v209, v209, 0xc0b8aa3b, v198
	v_fma_f32 v144, v200, v208, v204
	v_mfma_f32_32x32x16_f16 v[112:127], a[52:55], v[172:175], v[112:127]
	ds_read_b128 v[172:175], v192 offset:35840
	global_load_lds_dwordx4 v192, s[44:45] offset:3072 sc1
	v_rcp_f32_e32 v211, v211
	v_fmamk_f32 v210, v210, 0xc0b8aa3b, v198
	v_fma_f32 v145, v201, v209, v205
	v_mfma_f32_32x32x16_f16 v[96:111], a[56:59], v[176:179], v[96:111]
	ds_read_b128 v[176:179], v192 offset:36864
	v_rcp_f32_e32 v212, v212
	v_fmamk_f32 v211, v211, 0xc0b8aa3b, v198
	v_fma_f32 v146, v202, v210, v206
	v_mfma_f32_32x32x16_f16 v[112:127], a[56:59], v[180:183], v[112:127]
	ds_read_b128 v[180:183], v192 offset:37888
	v_rcp_f32_e32 v213, v213
	v_fma_f32 v147, v203, v211, v207
	s_waitcnt lgkmcnt(2)
	v_mfma_f32_32x32x16_f16 v[96:111], a[60:63], v[184:187], v[96:111]
	ds_read_b128 v[184:187], v192 offset:38912
	v_rcp_f32_e32 v214, v214
	v_mfma_f32_32x32x16_f16 v[112:127], a[60:63], v[188:191], v[112:127]
	ds_read_b128 v[188:191], v192 offset:39936
	s_mov_b32 m0, s58
	s_add_u32 s44, s34, 0x18000
	s_addc_u32 s45, s35, 0
	global_load_lds_dwordx4 v192, s[44:45] sc1
	v_rcp_f32_e32 v215, v215
	v_mfma_f32_32x32x16_f16 v[96:111], a[64:67], v[160:163], v[96:111]
	ds_read_b128 v[160:163], v192 offset:40960
	v_exp_f32_e32 v200, v144
	v_mfma_f32_32x32x16_f16 v[112:127], a[64:67], v[164:167], v[112:127]
	ds_read_b128 v[164:167], v192 offset:41984
	v_exp_f32_e32 v201, v145
	v_add_f32_e32 v200, 1.0, v200
	v_mfma_f32_32x32x16_f16 v[96:111], a[68:71], v[168:171], v[96:111]
	ds_read_b128 v[168:171], v192 offset:43008
	v_exp_f32_e32 v202, v146
	v_add_f32_e32 v201, 1.0, v201
	v_mfma_f32_32x32x16_f16 v[112:127], a[68:71], v[172:175], v[112:127]
	ds_read_b128 v[172:175], v192 offset:44032
	global_load_lds_dwordx4 v192, s[44:45] offset:1024 sc1
	v_exp_f32_e32 v203, v147
	v_add_f32_e32 v202, 1.0, v202
	s_waitcnt lgkmcnt(2)
	v_mfma_f32_32x32x16_f16 v[96:111], a[72:75], v[176:179], v[96:111]
	ds_read_b128 v[176:179], v192 offset:45056
	v_add_f32_e32 v203, 1.0, v203
	v_rcp_f32_e32 v200, v200
	v_mfma_f32_32x32x16_f16 v[112:127], a[72:75], v[180:183], v[112:127]
	ds_read_b128 v[180:183], v192 offset:46080
	v_rcp_f32_e32 v201, v201
	v_fma_f32 v200, v200, 2.0, -1.0
	v_mfma_f32_32x32x16_f16 v[96:111], a[76:79], v[184:187], v[96:111]
	ds_read_b128 v[184:187], v192 offset:47104
	v_rcp_f32_e32 v202, v202
	v_fma_f32 v201, v201, 2.0, -1.0
	v_mul_f32_e32 v216, v212, v200
	v_mfma_f32_32x32x16_f16 v[112:127], a[76:79], v[188:191], v[112:127]
	ds_read_b128 v[188:191], v192 offset:48128
	global_load_lds_dwordx4 v192, s[44:45] offset:2048 sc1
	v_rcp_f32_e32 v203, v203
	v_fma_f32 v202, v202, 2.0, -1.0
	v_mul_f32_e32 v217, v213, v201
	v_mfma_f32_32x32x16_f16 v[96:111], a[80:83], v[160:163], v[96:111]
	ds_read_b128 v[160:163], v192 offset:49152
	v_fma_f32 v203, v203, 2.0, -1.0
	v_mul_f32_e32 v218, v214, v202
	v_exp_f32_e32 v200, v80
	v_mfma_f32_32x32x16_f16 v[112:127], a[80:83], v[164:167], v[112:127]
	ds_read_b128 v[164:167], v192 offset:50176
	v_mul_f32_e32 v219, v215, v203
	v_cvt_pk_f16_f32 v220, v216, v217
	v_exp_f32_e32 v201, v81
	s_waitcnt lgkmcnt(2)
	v_mfma_f32_32x32x16_f16 v[96:111], a[84:87], v[168:171], v[96:111]
	ds_read_b128 v[168:171], v192 offset:51200
	v_cvt_pk_f16_f32 v221, v218, v219
	v_exp_f32_e32 v202, v82
	v_add_f32_e32 v200, 1.0, v200
	v_mfma_f32_32x32x16_f16 v[112:127], a[84:87], v[172:175], v[112:127]
	ds_read_b128 v[172:175], v192 offset:52224
	global_load_lds_dwordx4 v192, s[44:45] offset:3072 sc1
	s_cmp_eq_u32 s33, s60
	s_cbranch_scc1 .LE_ht42

.LE_join49:
	v_mfma_f32_32x32x16_f16 v[112:127], a[168:171], v[180:183], v[112:127]
	ds_read_b128 v[180:183], v193 offset:29696
	v_mfma_f32_32x32x16_f16 v[96:111], a[172:175], v[184:187], v[96:111]
	ds_read_b128 v[184:187], v193 offset:30720
	v_mfma_f32_32x32x16_f16 v[112:127], a[172:175], v[188:191], v[112:127]
	ds_read_b128 v[188:191], v193 offset:31744
	global_load_lds_dwordx4 v192, s[44:45] offset:2048 sc1
	s_waitcnt vmcnt(8)
	s_barrier
	v_mfma_f32_32x32x16_f16 v[96:111], a[176:179], v[160:163], v[96:111]
	ds_read_b128 v[160:163], v193 offset:32768
	v_mfma_f32_32x32x16_f16 v[112:127], a[176:179], v[164:167], v[112:127]
	ds_read_b128 v[164:167], v193 offset:33792
	s_waitcnt lgkmcnt(2)
	v_mfma_f32_32x32x16_f16 v[96:111], a[180:183], v[168:171], v[96:111]
	ds_read_b128 v[168:171], v193 offset:34816
	v_mfma_f32_32x32x16_f16 v[112:127], a[180:183], v[172:175], v[112:127]
	ds_read_b128 v[172:175], v193 offset:35840
	global_load_lds_dwordx4 v192, s[44:45] offset:3072 sc1
	v_mfma_f32_32x32x16_f16 v[96:111], a[184:187], v[176:179], v[96:111]
	ds_read_b128 v[176:179], v193 offset:36864
	v_mfma_f32_32x32x16_f16 v[112:127], a[184:187], v[180:183], v[112:127]
	ds_read_b128 v[180:183], v193 offset:37888
	v_mfma_f32_32x32x16_f16 v[96:111], a[188:191], v[184:187], v[96:111]
	ds_read_b128 v[184:187], v193 offset:38912
	v_mfma_f32_32x32x16_f16 v[112:127], a[188:191], v[188:191], v[112:127]
	ds_read_b128 v[188:191], v193 offset:39936
	s_mov_b32 m0, s54
	s_add_u32 s44, s34, 0x8000
	s_addc_u32 s45, s35, 0
	global_load_lds_dwordx4 v192, s[44:45] sc1
	s_waitcnt lgkmcnt(2)
	v_mfma_f32_32x32x16_f16 v[96:111], a[192:195], v[160:163], v[96:111]
	ds_read_b128 v[160:163], v193 offset:40960
	v_mfma_f32_32x32x16_f16 v[112:127], a[192:195], v[164:167], v[112:127]
	ds_read_b128 v[164:167], v193 offset:41984
	v_mfma_f32_32x32x16_f16 v[96:111], a[196:199], v[168:171], v[96:111]
	ds_read_b128 v[168:171], v193 offset:43008
	v_mfma_f32_32x32x16_f16 v[112:127], a[196:199], v[172:175], v[112:127]
	ds_read_b128 v[172:175], v193 offset:44032
	global_load_lds_dwordx4 v192, s[44:45] offset:1024 sc1
	v_mfma_f32_32x32x16_f16 v[96:111], a[200:203], v[176:179], v[96:111]
	ds_read_b128 v[176:179], v193 offset:45056
	v_mfma_f32_32x32x16_f16 v[112:127], a[200:203], v[180:183], v[112:127]
	ds_read_b128 v[180:183], v193 offset:46080
	s_waitcnt lgkmcnt(2)
	v_mfma_f32_32x32x16_f16 v[96:111], a[204:207], v[184:187], v[96:111]
	ds_read_b128 v[184:187], v193 offset:47104
	v_mfma_f32_32x32x16_f16 v[112:127], a[204:207], v[188:191], v[112:127]
	ds_read_b128 v[188:191], v193 offset:48128
	global_load_lds_dwordx4 v192, s[44:45] offset:2048 sc1
	s_waitcnt vmcnt(5)
	s_barrier
	v_mov_b32_e32 v199, 3
	s_cmp_eq_u32 s31, 0
	s_cbranch_scc1 .LE_slow50
	global_store_dword v197, v199, s[40:41]
.LE_join51:
	v_mfma_f32_32x32x16_f16 v[96:111], a[208:211], v[160:163], v[96:111]
	ds_read_b128 v[160:163], v193 offset:49152
	v_mfma_f32_32x32x16_f16 v[112:127], a[208:211], v[164:167], v[112:127]
	ds_read_b128 v[164:167], v193 offset:50176
	v_mfma_f32_32x32x16_f16 v[96:111], a[212:215], v[168:171], v[96:111]
	ds_read_b128 v[168:171], v193 offset:51200
	v_mfma_f32_32x32x16_f16 v[112:127], a[212:215], v[172:175], v[112:127]
	ds_read_b128 v[172:175], v193 offset:52224
	global_load_lds_dwordx4 v192, s[44:45] offset:3072 sc1
	s_waitcnt lgkmcnt(2)
	v_mfma_f32_32x32x16_f16 v[96:111], a[216:219], v[176:179], v[96:111]
	ds_read_b128 v[176:179], v193 offset:53248
	v_mfma_f32_32x32x16_f16 v[112:127], a[216:219], v[180:183], v[112:127]
	ds_read_b128 v[180:183], v193 offset:54272
	v_mfma_f32_32x32x16_f16 v[96:111], a[220:223], v[184:187], v[96:111]
	ds_read_b128 v[184:187], v193 offset:55296
	v_mfma_f32_32x32x16_f16 v[112:127], a[220:223], v[188:191], v[112:127]
	ds_read_b128 v[188:191], v193 offset:56320
	s_mov_b32 m0, s55
	s_add_u32 s44, s34, 0x9000
	s_addc_u32 s45, s35, 0
	global_load_lds_dwordx4 v192, s[44:45] sc1
	v_mfma_f32_32x32x16_f16 v[96:111], a[224:227], v[160:163], v[96:111]
	ds_read_b128 v[160:163], v193 offset:57344
	v_mfma_f32_32x32x16_f16 v[112:127], a[224:227], v[164:167], v[112:127]
	ds_read_b128 v[164:167], v193 offset:58368
	s_waitcnt lgkmcnt(2)
	v_mfma_f32_32x32x16_f16 v[96:111], a[228:231], v[168:171], v[96:111]
	ds_read_b128 v[168:171], v193 offset:59392
	v_mfma_f32_32x32x16_f16 v[112:127], a[228:231], v[172:175], v[112:127]
	ds_read_b128 v[172:175], v193 offset:60416
	global_load_lds_dwordx4 v192, s[44:45] offset:1024 sc1
	v_mfma_f32_32x32x16_f16 v[96:111], a[232:235], v[176:179], v[96:111]
	ds_read_b128 v[176:179], v193 offset:61440
	v_mfma_f32_32x32x16_f16 v[112:127], a[232:235], v[180:183], v[112:127]
	ds_read_b128 v[180:183], v193 offset:62464
	v_mfma_f32_32x32x16_f16 v[96:111], a[236:239], v[184:187], v[96:111]
	ds_read_b128 v[184:187], v193 offset:63488
	v_mfma_f32_32x32x16_f16 v[112:127], a[236:239], v[188:191], v[112:127]
	ds_read_b128 v[188:191], v193 offset:64512
	global_load_lds_dwordx4 v192, s[44:45] offset:2048 sc1
	s_waitcnt vmcnt(8)
	s_barrier
	s_waitcnt lgkmcnt(2)
	v_mfma_f32_32x32x16_f16 v[96:111], a[240:243], v[160:163], v[96:111]
	ds_read_b128 v[160:163], v192 offset:0
	v_mfma_f32_32x32x16_f16 v[112:127], a[240:243], v[164:167], v[112:127]
	ds_read_b128 v[164:167], v192 offset:1024
	v_mfma_f32_32x32x16_f16 v[96:111], a[244:247], v[168:171], v[96:111]
	ds_read_b128 v[168:171], v192 offset:2048
	v_mfma_f32_32x32x16_f16 v[112:127], a[244:247], v[172:175], v[112:127]
	ds_read_b128 v[172:175], v192 offset:3072
	global_load_lds_dwordx4 v192, s[44:45] offset:3072 sc1
	v_mfma_f32_32x32x16_f16 v[96:111], a[248:251], v[176:179], v[96:111]
	ds_read_b128 v[176:179], v192 offset:4096
	v_mfma_f32_32x32x16_f16 v[112:127], a[248:251], v[180:183], v[112:127]
	ds_read_b128 v[180:183], v192 offset:5120
	s_waitcnt lgkmcnt(2)
	v_mfma_f32_32x32x16_f16 v[96:111], a[252:255], v[184:187], v[96:111]
	ds_read_b128 v[184:187], v192 offset:6144
	v_mfma_f32_32x32x16_f16 v[112:127], a[252:255], v[188:191], v[112:127]
	ds_read_b128 v[188:191], v192 offset:7168
	s_mov_b32 m0, s56
	s_add_u32 s44, s34, 0x10000
	s_addc_u32 s45, s35, 0
	global_load_lds_dwordx4 v192, s[44:45] sc1
	s_add_u32 s33, s33, 1
	s_cmp_lt_u32 s33, s28
	s_cbranch_scc1 .LE_loop12

.LD_join19:
	s_waitcnt lgkmcnt(3)
	v_mfma_f32_32x32x16_f16 v[0:15], a[180:183], v[168:171], v[0:15]
	ds_read_b128 v[168:171], v193 offset:34816
	v_mfma_f32_32x32x16_f16 v[16:31], a[180:183], v[172:175], v[16:31]
	ds_read_b128 v[172:175], v193 offset:35840
	global_load_lds_dwordx4 v192, s[44:45] offset:3072 sc1
	v_mfma_f32_32x32x16_f16 v[0:15], a[184:187], v[176:179], v[0:15]
	ds_read_b128 v[176:179], v193 offset:36864
	v_mfma_f32_32x32x16_f16 v[16:31], a[184:187], v[180:183], v[16:31]
	ds_read_b128 v[180:183], v193 offset:37888
	v_mfma_f32_32x32x16_f16 v[0:15], a[188:191], v[184:187], v[0:15]
	ds_read_b128 v[184:187], v193 offset:38912
	v_mfma_f32_32x32x16_f16 v[16:31], a[188:191], v[188:191], v[16:31]
	ds_read_b128 v[188:191], v193 offset:39936
	s_mov_b32 m0, s54
	s_add_u32 s44, s34, 0x8000
	s_addc_u32 s45, s35, 0
	global_load_lds_dwordx4 v192, s[44:45] sc1
	s_waitcnt lgkmcnt(2)
	v_mfma_f32_32x32x16_f16 v[0:15], a[192:195], v[160:163], v[0:15]
	ds_read_b128 v[160:163], v193 offset:40960
	v_mfma_f32_32x32x16_f16 v[16:31], a[192:195], v[164:167], v[16:31]
	ds_read_b128 v[164:167], v193 offset:41984
	v_mfma_f32_32x32x16_f16 v[0:15], a[196:199], v[168:171], v[0:15]
	ds_read_b128 v[168:171], v193 offset:43008
	v_mfma_f32_32x32x16_f16 v[16:31], a[196:199], v[172:175], v[16:31]
	ds_read_b128 v[172:175], v193 offset:44032
	global_load_lds_dwordx4 v192, s[44:45] offset:1024 sc1
	v_mfma_f32_32x32x16_f16 v[0:15], a[200:203], v[176:179], v[0:15]
	ds_read_b128 v[176:179], v193 offset:45056
	v_mfma_f32_32x32x16_f16 v[16:31], a[200:203], v[180:183], v[16:31]
	ds_read_b128 v[180:183], v193 offset:46080
	s_waitcnt lgkmcnt(2)
	v_mfma_f32_32x32x16_f16 v[0:15], a[204:207], v[184:187], v[0:15]
	ds_read_b128 v[184:187], v193 offset:47104
	v_mfma_f32_32x32x16_f16 v[16:31], a[204:207], v[188:191], v[16:31]
	ds_read_b128 v[188:191], v193 offset:48128
	global_load_lds_dwordx4 v192, s[44:45] offset:2048 sc1
	v_mfma_f32_32x32x16_f16 v[0:15], a[208:211], v[160:163], v[0:15]
	ds_read_b128 v[160:163], v193 offset:49152
	v_mfma_f32_32x32x16_f16 v[16:31], a[208:211], v[164:167], v[16:31]
	ds_read_b128 v[164:167], v193 offset:50176
	v_mfma_f32_32x32x16_f16 v[0:15], a[212:215], v[168:171], v[0:15]
	ds_read_b128 v[168:171], v193 offset:51200
	v_mfma_f32_32x32x16_f16 v[16:31], a[212:215], v[172:175], v[16:31]
	ds_read_b128 v[172:175], v193 offset:52224
	global_load_lds_dwordx4 v192, s[44:45] offset:3072 sc1
	s_waitcnt lgkmcnt(2)
	v_mfma_f32_32x32x16_f16 v[0:15], a[216:219], v[176:179], v[0:15]
	ds_read_b128 v[176:179], v193 offset:53248
	s_waitcnt vmcnt(5)
	s_barrier
	v_mov_b32_e32 v199, 4
	s_cmp_eq_u32 s31, 0
	s_cbranch_scc1 .LD_slow20
	global_store_dword v197, v199, s[40:41]
.LD_join21:
	ds_read_b64 v[200:201], v249 offset:1536
	ds_read_b64 v[202:203], v249 offset:3584
	ds_read_b64 v[204:205], v249 offset:5632
	ds_read_b64 v[206:207], v249 offset:7680
	v_mfma_f32_32x32x16_f16 v[16:31], a[216:219], v[180:183], v[16:31]
	ds_read_b128 v[180:183], v193 offset:54272
	v_mfma_f32_32x32x16_f16 v[0:15], a[220:223], v[184:187], v[0:15]
	ds_read_b128 v[184:187], v193 offset:55296
	v_mfma_f32_32x32x16_f16 v[16:31], a[220:223], v[188:191], v[16:31]
	ds_read_b128 v[188:191], v193 offset:56320
	s_mov_b32 m0, s55
	s_add_u32 s44, s34, 0x9000
	s_addc_u32 s45, s35, 0
	global_load_lds_dwordx4 v192, s[44:45] sc1
	v_mfma_f32_32x32x16_f16 v[0:15], a[224:227], v[160:163], v[0:15]
	ds_read_b128 v[160:163], v193 offset:57344
	v_mfma_f32_32x32x16_f16 v[16:31], a[224:227], v[164:167], v[16:31]
	ds_read_b128 v[164:167], v193 offset:58368
	s_waitcnt lgkmcnt(2)
	v_mfma_f32_32x32x16_f16 v[0:15], a[228:231], v[168:171], v[0:15]
	ds_read_b128 v[168:171], v193 offset:59392
	v_mfma_f32_32x32x16_f16 v[16:31], a[228:231], v[172:175], v[16:31]
	ds_read_b128 v[172:175], v193 offset:60416
	global_load_lds_dwordx4 v192, s[44:45] offset:1024 sc1
	v_mfma_f32_32x32x16_f16 v[0:15], a[232:235], v[176:179], v[0:15]
	ds_read_b128 v[176:179], v193 offset:61440
	v_mfma_f32_32x32x16_f16 v[16:31], a[232:235], v[180:183], v[16:31]
	ds_read_b128 v[180:183], v193 offset:62464
	v_mfma_f32_32x32x16_f16 v[0:15], a[236:239], v[184:187], v[0:15]
	ds_read_b128 v[184:187], v193 offset:63488
	v_mfma_f32_32x32x16_f16 v[16:31], a[236:239], v[188:191], v[16:31]
	ds_read_b128 v[188:191], v193 offset:64512
	global_load_lds_dwordx4 v192, s[44:45] offset:2048 sc1
	s_waitcnt vmcnt(8)
	s_barrier
	s_waitcnt lgkmcnt(2)
	v_mfma_f32_32x32x16_f16 v[0:15], a[240:243], v[160:163], v[0:15]
	ds_read_b128 v[160:163], v192 offset:0
	v_add_f32_e32 v200, v200, v202
	v_add_f32_e32 v201, v201, v203
	v_add_f32_e32 v200, v200, v204
	v_add_f32_e32 v201, v201, v205
	v_add_f32_e32 v200, v200, v206
	v_add_f32_e32 v201, v201, v207
	global_store_dwordx2 v250, v[200:201], s[72:73]
	v_mfma_f32_32x32x16_f16 v[16:31], a[240:243], v[164:167], v[16:31]
	ds_read_b128 v[164:167], v192 offset:1024
	v_mfma_f32_32x32x16_f16 v[0:15], a[244:247], v[168:171], v[0:15]
	ds_read_b128 v[168:171], v192 offset:2048
	v_mfma_f32_32x32x16_f16 v[16:31], a[244:247], v[172:175], v[16:31]
	ds_read_b128 v[172:175], v192 offset:3072
	global_load_lds_dwordx4 v192, s[44:45] offset:3072 sc1
	v_mfma_f32_32x32x16_f16 v[0:15], a[248:251], v[176:179], v[0:15]
	ds_read_b128 v[176:179], v192 offset:4096
	s_and_b32 s64, s33, 1
	s_lshl_b32 s64, s64, 22
	s_add_u32 s64, s64, s50
	s_add_u32 s36, s6, s64
	s_addc_u32 s37, s7, 0
	s_lshl_b32 s64, s33, 3
	s_add_u32 s64, s64, s29
	s_lshl_b32 s64, s64, 5
	s_add_u32 s64, s64, s30
	s_lshl_b32 s64, s64, 2
	s_add_u32 s40, s8, s64
	s_addc_u32 s41, s9, 0
	s_lshl_b32 s64, s33, 19
	s_add_u32 s72, s62, s64
	s_addc_u32 s73, s63, 0
	v_mfma_f32_32x32x16_f16 v[16:31], a[248:251], v[180:183], v[16:31]
	ds_read_b128 v[180:183], v192 offset:5120
	s_waitcnt lgkmcnt(2)
	v_mfma_f32_32x32x16_f16 v[0:15], a[252:255], v[184:187], v[0:15]
	ds_read_b128 v[184:187], v192 offset:6144
	v_mfma_f32_32x32x16_f16 v[16:31], a[252:255], v[188:191], v[16:31]
	ds_read_b128 v[188:191], v192 offset:7168
	s_mov_b32 m0, s56
	s_add_u32 s44, s34, 0x10000
	s_addc_u32 s45, s35, 0
	global_load_lds_dwordx4 v192, s[44:45] sc1
	s_nop 3
	s_waitcnt lgkmcnt(2)
	v_mfma_f32_32x32x16_f16 v[32:47], a[0:3], v[160:163], v[32:47]
	ds_read_b128 v[160:163], v192 offset:8192
	v_exp_f32_e32 v200, v0
	v_mfma_f32_32x32x16_f16 v[48:63], a[0:3], v[164:167], v[48:63]
	ds_read_b128 v[164:167], v192 offset:9216
	s_lshl_b32 s64, s71, 3
	s_add_u32 s64, s64, s29
	s_lshl_b32 s64, s64, 7
	s_add_u32 s38, s8, s64
	s_addc_u32 s39, s9, 0
	global_load_dword v251, v196, s[38:39] sc1
	v_exp_f32_e32 v201, v1
	v_add_f32_e32 v200, 1.0, v200
	v_mfma_f32_32x32x16_f16 v[32:47], a[4:7], v[168:171], v[32:47]
	ds_read_b128 v[168:171], v192 offset:10240
	v_exp_f32_e32 v202, v2
	v_add_f32_e32 v201, 1.0, v201
	v_mfma_f32_32x32x16_f16 v[48:63], a[4:7], v[172:175], v[48:63]
	ds_read_b128 v[172:175], v192 offset:11264
	global_load_lds_dwordx4 v192, s[44:45] offset:1024 sc1
	v_exp_f32_e32 v203, v3
	v_add_f32_e32 v202, 1.0, v202
	v_mfma_f32_32x32x16_f16 v[32:47], a[8:11], v[176:179], v[32:47]
	ds_read_b128 v[176:179], v192 offset:12288
	v_exp_f32_e32 v204, v4
	v_add_f32_e32 v203, 1.0, v203
	v_mfma_f32_32x32x16_f16 v[48:63], a[8:11], v[180:183], v[48:63]
	ds_read_b128 v[180:183], v192 offset:13312
	v_exp_f32_e32 v205, v5
	v_add_f32_e32 v204, 1.0, v204
	s_waitcnt lgkmcnt(2)
	v_mfma_f32_32x32x16_f16 v[32:47], a[12:15], v[184:187], v[32:47]
	ds_read_b128 v[184:187], v192 offset:14336
	v_exp_f32_e32 v206, v6
	v_add_f32_e32 v205, 1.0, v205
	v_mfma_f32_32x32x16_f16 v[48:63], a[12:15], v[188:191], v[48:63]
	ds_read_b128 v[188:191], v192 offset:15360
	global_load_lds_dwordx4 v192, s[44:45] offset:2048 sc1
	v_exp_f32_e32 v207, v7
	v_add_f32_e32 v206, 1.0, v206
	v_mfma_f32_32x32x16_f16 v[32:47], a[16:19], v[160:163], v[32:47]
	ds_read_b128 v[160:163], v192 offset:16384
	v_exp_f32_e32 v208, v8
	v_add_f32_e32 v207, 1.0, v207
	v_mfma_f32_32x32x16_f16 v[48:63], a[16:19], v[164:167], v[48:63]
	ds_read_b128 v[164:167], v192 offset:17408
	v_exp_f32_e32 v209, v9
	v_add_f32_e32 v208, 1.0, v208
	v_mfma_f32_32x32x16_f16 v[32:47], a[20:23], v[168:171], v[32:47]
	ds_read_b128 v[168:171], v192 offset:18432
	v_exp_f32_e32 v210, v10
	v_add_f32_e32 v209, 1.0, v209
	v_mfma_f32_32x32x16_f16 v[48:63], a[20:23], v[172:175], v[48:63]
	ds_read_b128 v[172:175], v192 offset:19456
	global_load_lds_dwordx4 v192, s[44:45] offset:3072 sc1
	v_exp_f32_e32 v211, v11
	v_add_f32_e32 v210, 1.0, v210
	s_waitcnt lgkmcnt(2)
	v_mfma_f32_32x32x16_f16 v[32:47], a[24:27], v[176:179], v[32:47]
	ds_read_b128 v[176:179], v192 offset:20480
	v_exp_f32_e32 v212, v12
	v_add_f32_e32 v211, 1.0, v211
	v_mfma_f32_32x32x16_f16 v[48:63], a[24:27], v[180:183], v[48:63]
	ds_read_b128 v[180:183], v192 offset:21504
	v_exp_f32_e32 v213, v13
	v_add_f32_e32 v212, 1.0, v212
	v_mfma_f32_32x32x16_f16 v[32:47], a[28:31], v[184:187], v[32:47]
	ds_read_b128 v[184:187], v192 offset:22528
	v_exp_f32_e32 v214, v14
	v_add_f32_e32 v213, 1.0, v213
	v_mfma_f32_32x32x16_f16 v[48:63], a[28:31], v[188:191], v[48:63]
	ds_read_b128 v[188:191], v192 offset:23552
	s_mov_b32 m0, s57
	s_add_u32 s44, s34, 0x11000
	s_addc_u32 s45, s35, 0
	global_load_lds_dwordx4 v192, s[44:45] sc1
	v_exp_f32_e32 v215, v15
	v_add_f32_e32 v214, 1.0, v214
	v_mfma_f32_32x32x16_f16 v[32:47], a[32:35], v[160:163], v[32:47]
	ds_read_b128 v[160:163], v192 offset:24576
	v_add_f32_e32 v215, 1.0, v215
	v_rcp_f32_e32 v200, v200
	v_mfma_f32_32x32x16_f16 v[48:63], a[32:35], v[164:167], v[48:63]
	ds_read_b128 v[164:167], v192 offset:25600
	v_rcp_f32_e32 v201, v201
	s_waitcnt lgkmcnt(2)
	v_mfma_f32_32x32x16_f16 v[32:47], a[36:39], v[168:171], v[32:47]
	ds_read_b128 v[168:171], v192 offset:26624
	v_rcp_f32_e32 v202, v202
	v_mfma_f32_32x32x16_f16 v[48:63], a[36:39], v[172:175], v[48:63]
	ds_read_b128 v[172:175], v192 offset:27648
	global_load_lds_dwordx4 v192, s[44:45] offset:1024 sc1
	v_rcp_f32_e32 v203, v203
	v_mfma_f32_32x32x16_f16 v[32:47], a[40:43], v[176:179], v[32:47]
	ds_read_b128 v[176:179], v192 offset:28672
	v_rcp_f32_e32 v204, v204
	v_mfma_f32_32x32x16_f16 v[48:63], a[40:43], v[180:183], v[48:63]
	ds_read_b128 v[180:183], v192 offset:29696
	v_rcp_f32_e32 v205, v205
	v_mul_f32_e32 v204, v204, v128
	v_mfma_f32_32x32x16_f16 v[32:47], a[44:47], v[184:187], v[32:47]
	ds_read_b128 v[184:187], v192 offset:30720
	v_rcp_f32_e32 v206, v206
	v_mul_f32_e32 v205, v205, v129
	v_mfma_f32_32x32x16_f16 v[48:63], a[44:47], v[188:191], v[48:63]
	ds_read_b128 v[188:191], v192 offset:31744
	global_load_lds_dwordx4 v192, s[44:45] offset:2048 sc1
	v_rcp_f32_e32 v207, v207
	v_mul_f32_e32 v206, v206, v130
	s_waitcnt vmcnt(8)
	s_barrier
	s_waitcnt lgkmcnt(2)
	v_mfma_f32_32x32x16_f16 v[32:47], a[48:51], v[160:163], v[32:47]
	ds_read_b128 v[160:163], v192 offset:32768
	v_rcp_f32_e32 v208, v208
	v_mul_f32_e32 v207, v207, v131
	v_mfma_f32_32x32x16_f16 v[48:63], a[48:51], v[164:167], v[48:63]
	ds_read_b128 v[164:167], v192 offset:33792
	v_rcp_f32_e32 v209, v209
	v_fmamk_f32 v208, v208, 0xc0b8aa3b, v198
	v_mfma_f32_32x32x16_f16 v[32:47], a[52:55], v[168:171], v[32:47]
	ds_read_b128 v[168:171], v192 offset:34816
	v_rcp_f32_e32 v210, v210
	v_fmamk_f32 v209, v209, 0xc0b8aa3b, v198
	v_fma_f32 v128, v200, v208, v204
	v_mfma_f32_32x32x16_f16 v[48:63], a[52:55], v[172:175], v[48:63]
	ds_read_b128 v[172:175], v192 offset:35840
	global_load_lds_dwordx4 v192, s[44:45] offset:3072 sc1
	v_rcp_f32_e32 v211, v211
	v_fmamk_f32 v210, v210, 0xc0b8aa3b, v198
	v_fma_f32 v129, v201, v209, v205
	v_mfma_f32_32x32x16_f16 v[32:47], a[56:59], v[176:179], v[32:47]
	ds_read_b128 v[176:179], v192 offset:36864
	v_rcp_f32_e32 v212, v212
	v_fmamk_f32 v211, v211, 0xc0b8aa3b, v198
	v_fma_f32 v130, v202, v210, v206
	v_mfma_f32_32x32x16_f16 v[48:63], a[56:59], v[180:183], v[48:63]
	ds_read_b128 v[180:183], v192 offset:37888
	v_rcp_f32_e32 v213, v213
	v_fma_f32 v131, v203, v211, v207
	s_waitcnt lgkmcnt(2)
	v_mfma_f32_32x32x16_f16 v[32:47], a[60:63], v[184:187], v[32:47]
	ds_read_b128 v[184:187], v192 offset:38912
	v_rcp_f32_e32 v214, v214
	v_mfma_f32_32x32x16_f16 v[48:63], a[60:63], v[188:191], v[48:63]
	ds_read_b128 v[188:191], v192 offset:39936
	s_mov_b32 m0, s58
	s_add_u32 s44, s34, 0x18000
	s_addc_u32 s45, s35, 0
	global_load_lds_dwordx4 v192, s[44:45] sc1
	v_rcp_f32_e32 v215, v215
	v_mfma_f32_32x32x16_f16 v[32:47], a[64:67], v[160:163], v[32:47]
	ds_read_b128 v[160:163], v192 offset:40960
	v_exp_f32_e32 v200, v128
	v_mfma_f32_32x32x16_f16 v[48:63], a[64:67], v[164:167], v[48:63]
	ds_read_b128 v[164:167], v192 offset:41984
	v_exp_f32_e32 v201, v129
	v_add_f32_e32 v200, 1.0, v200
	v_mfma_f32_32x32x16_f16 v[32:47], a[68:71], v[168:171], v[32:47]
	ds_read_b128 v[168:171], v192 offset:43008
	v_exp_f32_e32 v202, v130
	v_add_f32_e32 v201, 1.0, v201
	v_mfma_f32_32x32x16_f16 v[48:63], a[68:71], v[172:175], v[48:63]
	ds_read_b128 v[172:175], v192 offset:44032
	global_load_lds_dwordx4 v192, s[44:45] offset:1024 sc1
	v_exp_f32_e32 v203, v131
	v_add_f32_e32 v202, 1.0, v202
	s_waitcnt lgkmcnt(2)
	v_mfma_f32_32x32x16_f16 v[32:47], a[72:75], v[176:179], v[32:47]
	ds_read_b128 v[176:179], v192 offset:45056
	v_add_f32_e32 v203, 1.0, v203
	v_rcp_f32_e32 v200, v200
	v_mfma_f32_32x32x16_f16 v[48:63], a[72:75], v[180:183], v[48:63]
	ds_read_b128 v[180:183], v192 offset:46080
	v_rcp_f32_e32 v201, v201
	v_fma_f32 v200, v200, 2.0, -1.0
	v_mfma_f32_32x32x16_f16 v[32:47], a[76:79], v[184:187], v[32:47]
	ds_read_b128 v[184:187], v192 offset:47104
	v_rcp_f32_e32 v202, v202
	v_fma_f32 v201, v201, 2.0, -1.0
	v_mul_f32_e32 v216, v212, v200
	v_mfma_f32_32x32x16_f16 v[48:63], a[76:79], v[188:191], v[48:63]
	ds_read_b128 v[188:191], v192 offset:48128
	global_load_lds_dwordx4 v192, s[44:45] offset:2048 sc1
	v_rcp_f32_e32 v203, v203
	v_fma_f32 v202, v202, 2.0, -1.0
	v_mul_f32_e32 v217, v213, v201
	v_mfma_f32_32x32x16_f16 v[32:47], a[80:83], v[160:163], v[32:47]
	ds_read_b128 v[160:163], v192 offset:49152
	v_fma_f32 v203, v203, 2.0, -1.0
	v_mul_f32_e32 v218, v214, v202
	v_exp_f32_e32 v200, v16
	v_mfma_f32_32x32x16_f16 v[48:63], a[80:83], v[164:167], v[48:63]
	ds_read_b128 v[164:167], v192 offset:50176
	v_mul_f32_e32 v219, v215, v203
	v_mul_f32_e32 v236, v216, v228
	v_exp_f32_e32 v201, v17
	s_waitcnt lgkmcnt(2)
	v_mfma_f32_32x32x16_f16 v[32:47], a[84:87], v[168:171], v[32:47]
	ds_read_b128 v[168:171], v192 offset:51200
	v_mul_f32_e32 v237, v216, v232
	v_fmac_f32_e32 v236, v217, v229
	v_exp_f32_e32 v202, v18
	v_mfma_f32_32x32x16_f16 v[48:63], a[84:87], v[172:175], v[48:63]
	ds_read_b128 v[172:175], v192 offset:52224
	global_load_lds_dwordx4 v192, s[44:45] offset:3072 sc1
	v_fmac_f32_e32 v237, v217, v233
	v_fmac_f32_e32 v236, v218, v230
	v_exp_f32_e32 v203, v19
	v_mfma_f32_32x32x16_f16 v[32:47], a[88:91], v[176:179], v[32:47]
	ds_read_b128 v[176:179], v192 offset:53248
	v_fmac_f32_e32 v237, v218, v234
	v_fmac_f32_e32 v236, v219, v231
	v_exp_f32_e32 v204, v20
	v_mfma_f32_32x32x16_f16 v[48:63], a[88:91], v[180:183], v[48:63]
	ds_read_b128 v[180:183], v192 offset:54272
	v_fmac_f32_e32 v237, v219, v235
	v_mov_b32_e32 v238, v236
	v_exp_f32_e32 v205, v21
	v_mfma_f32_32x32x16_f16 v[32:47], a[92:95], v[184:187], v[32:47]
	ds_read_b128 v[184:187], v192 offset:55296
	v_mov_b32_e32 v240, v237
	v_cvt_pk_f16_f32 v220, v216, v217
	v_exp_f32_e32 v206, v22
	v_mfma_f32_32x32x16_f16 v[48:63], a[92:95], v[188:191], v[48:63]
	ds_read_b128 v[188:191], v192 offset:56320
	s_mov_b32 m0, s59
	s_add_u32 s44, s34, 0x19000
	s_addc_u32 s45, s35, 0
	global_load_lds_dwordx4 v192, s[44:45] sc1
	v_permlane32_swap_b32_e32 v236, v238
	v_permlane32_swap_b32_e32 v237, v240
	v_add_f32_e32 v238, v236, v238
	v_add_f32_e32 v239, v237, v240
	ds_write_b64 v248, v[238:239] offset:0
	v_exp_f32_e32 v207, v23
	s_waitcnt lgkmcnt(3)
	v_mfma_f32_32x32x16_f16 v[32:47], a[96:99], v[160:163], v[32:47]
	ds_read_b128 v[160:163], v192 offset:57344
	v_cvt_pk_f16_f32 v221, v218, v219
	v_exp_f32_e32 v208, v24
	v_add_f32_e32 v200, 1.0, v200
	v_mfma_f32_32x32x16_f16 v[48:63], a[96:99], v[164:167], v[48:63]
	ds_read_b128 v[164:167], v192 offset:58368
	v_exp_f32_e32 v209, v25
	v_add_f32_e32 v201, 1.0, v201
	v_add_f32_e32 v202, 1.0, v202
	v_mfma_f32_32x32x16_f16 v[32:47], a[100:103], v[168:171], v[32:47]
	ds_read_b128 v[168:171], v192 offset:59392
	v_exp_f32_e32 v210, v26
	v_add_f32_e32 v203, 1.0, v203
	v_add_f32_e32 v204, 1.0, v204
	v_mfma_f32_32x32x16_f16 v[48:63], a[100:103], v[172:175], v[48:63]
	ds_read_b128 v[172:175], v192 offset:60416
	global_load_lds_dwordx4 v192, s[44:45] offset:1024 sc1
	v_exp_f32_e32 v211, v27
	v_add_f32_e32 v205, 1.0, v205
	v_add_f32_e32 v206, 1.0, v206
	v_mfma_f32_32x32x16_f16 v[32:47], a[104:107], v[176:179], v[32:47]
	ds_read_b128 v[176:179], v192 offset:61440
	v_exp_f32_e32 v212, v28
	v_add_f32_e32 v207, 1.0, v207
	v_add_f32_e32 v208, 1.0, v208
	v_mfma_f32_32x32x16_f16 v[48:63], a[104:107], v[180:183], v[48:63]
	ds_read_b128 v[180:183], v192 offset:62464
	v_exp_f32_e32 v213, v29
	v_add_f32_e32 v209, 1.0, v209
	v_add_f32_e32 v210, 1.0, v210
	s_waitcnt lgkmcnt(2)
	v_mfma_f32_32x32x16_f16 v[32:47], a[108:111], v[184:187], v[32:47]
	ds_read_b128 v[184:187], v192 offset:63488
	v_exp_f32_e32 v214, v30
	v_add_f32_e32 v211, 1.0, v211
	v_add_f32_e32 v212, 1.0, v212
	v_mfma_f32_32x32x16_f16 v[48:63], a[108:111], v[188:191], v[48:63]
	ds_read_b128 v[188:191], v192 offset:64512
	global_load_lds_dwordx4 v192, s[44:45] offset:2048 sc1
	v_exp_f32_e32 v215, v31
	v_add_f32_e32 v213, 1.0, v213
	v_add_f32_e32 v214, 1.0, v214
	s_waitcnt vmcnt(7)
	s_barrier
	v_mfma_f32_32x32x16_f16 v[32:47], a[112:115], v[160:163], v[32:47]
	ds_read_b128 v[160:163], v193 offset:0
	v_add_f32_e32 v215, 1.0, v215
	v_rcp_f32_e32 v200, v200
	v_mfma_f32_32x32x16_f16 v[48:63], a[112:115], v[164:167], v[48:63]
	ds_read_b128 v[164:167], v193 offset:1024
	v_rcp_f32_e32 v201, v201
	v_mfma_f32_32x32x16_f16 v[32:47], a[116:119], v[168:171], v[32:47]
	ds_read_b128 v[168:171], v193 offset:2048
	v_rcp_f32_e32 v202, v202
	v_mfma_f32_32x32x16_f16 v[48:63], a[116:119], v[172:175], v[48:63]
	ds_read_b128 v[172:175], v193 offset:3072
	global_load_lds_dwordx4 v192, s[44:45] offset:3072 sc1
	v_rcp_f32_e32 v203, v203
	s_waitcnt lgkmcnt(2)
	v_mfma_f32_32x32x16_f16 v[32:47], a[120:123], v[176:179], v[32:47]
	ds_read_b128 v[176:179], v193 offset:4096
	v_rcp_f32_e32 v204, v204
	s_add_u32 s46, s42, 0x6000
	s_addc_u32 s47, s43, 0
	global_load_dwordx4 v[96:99], v192, s[46:47] offset:0
	v_mfma_f32_32x32x16_f16 v[48:63], a[120:123], v[180:183], v[48:63]
	ds_read_b128 v[180:183], v193 offset:5120
	v_rcp_f32_e32 v205, v205
	v_mul_f32_e32 v204, v204, v132
	global_load_dwordx4 v[100:103], v192, s[46:47] offset:1024
	global_load_dwordx4 v[104:107], v192, s[46:47] offset:2048
	v_mfma_f32_32x32x16_f16 v[32:47], a[124:127], v[184:187], v[32:47]
	ds_read_b128 v[184:187], v193 offset:6144
	v_rcp_f32_e32 v206, v206
	v_mul_f32_e32 v205, v205, v133
	global_load_dwordx4 v[108:111], v192, s[46:47] offset:3072
	s_add_u32 s46, s42, 0x7000
	s_addc_u32 s47, s43, 0
	v_mfma_f32_32x32x16_f16 v[48:63], a[124:127], v[188:191], v[48:63]
	ds_read_b128 v[188:191], v193 offset:7168
	v_cmp_gt_u32_e32 vcc, 3, v251
	s_cbranch_vccnz .LD_tpoll23

.LD_join25:
	s_waitcnt lgkmcnt(3)
	v_mfma_f32_32x32x16_f16 v[32:47], a[180:183], v[168:171], v[32:47]
	ds_read_b128 v[168:171], v193 offset:34816
	v_mfma_f32_32x32x16_f16 v[48:63], a[180:183], v[172:175], v[48:63]
	ds_read_b128 v[172:175], v193 offset:35840
	global_load_lds_dwordx4 v192, s[44:45] offset:3072 sc1
	v_mfma_f32_32x32x16_f16 v[32:47], a[184:187], v[176:179], v[32:47]
	ds_read_b128 v[176:179], v193 offset:36864
	v_mfma_f32_32x32x16_f16 v[48:63], a[184:187], v[180:183], v[48:63]
	ds_read_b128 v[180:183], v193 offset:37888
	v_mfma_f32_32x32x16_f16 v[32:47], a[188:191], v[184:187], v[32:47]
	ds_read_b128 v[184:187], v193 offset:38912
	v_mfma_f32_32x32x16_f16 v[48:63], a[188:191], v[188:191], v[48:63]
	ds_read_b128 v[188:191], v193 offset:39936
	s_mov_b32 m0, s54
	s_add_u32 s44, s34, 0x8000
	s_addc_u32 s45, s35, 0
	global_load_lds_dwordx4 v192, s[44:45] sc1
	s_waitcnt lgkmcnt(2)
	v_mfma_f32_32x32x16_f16 v[32:47], a[192:195], v[160:163], v[32:47]
	ds_read_b128 v[160:163], v193 offset:40960
	v_mfma_f32_32x32x16_f16 v[48:63], a[192:195], v[164:167], v[48:63]
	ds_read_b128 v[164:167], v193 offset:41984
	v_mfma_f32_32x32x16_f16 v[32:47], a[196:199], v[168:171], v[32:47]
	ds_read_b128 v[168:171], v193 offset:43008
	v_mfma_f32_32x32x16_f16 v[48:63], a[196:199], v[172:175], v[48:63]
	ds_read_b128 v[172:175], v193 offset:44032
	global_load_lds_dwordx4 v192, s[44:45] offset:1024 sc1
	v_mfma_f32_32x32x16_f16 v[32:47], a[200:203], v[176:179], v[32:47]
	ds_read_b128 v[176:179], v193 offset:45056
	v_mfma_f32_32x32x16_f16 v[48:63], a[200:203], v[180:183], v[48:63]
	ds_read_b128 v[180:183], v193 offset:46080
	s_waitcnt lgkmcnt(2)
	v_mfma_f32_32x32x16_f16 v[32:47], a[204:207], v[184:187], v[32:47]
	ds_read_b128 v[184:187], v193 offset:47104
	v_mfma_f32_32x32x16_f16 v[48:63], a[204:207], v[188:191], v[48:63]
	ds_read_b128 v[188:191], v193 offset:48128
	global_load_lds_dwordx4 v192, s[44:45] offset:2048 sc1
	v_mfma_f32_32x32x16_f16 v[32:47], a[208:211], v[160:163], v[32:47]
	ds_read_b128 v[160:163], v193 offset:49152
	v_mfma_f32_32x32x16_f16 v[48:63], a[208:211], v[164:167], v[48:63]
	ds_read_b128 v[164:167], v193 offset:50176
	v_mfma_f32_32x32x16_f16 v[32:47], a[212:215], v[168:171], v[32:47]
	ds_read_b128 v[168:171], v193 offset:51200
	v_mfma_f32_32x32x16_f16 v[48:63], a[212:215], v[172:175], v[48:63]
	ds_read_b128 v[172:175], v193 offset:52224
	global_load_lds_dwordx4 v192, s[44:45] offset:3072 sc1
	s_waitcnt lgkmcnt(2)
	v_mfma_f32_32x32x16_f16 v[32:47], a[216:219], v[176:179], v[32:47]
	ds_read_b128 v[176:179], v193 offset:53248
	s_waitcnt vmcnt(5)
	s_barrier
	v_mov_b32_e32 v199, 1
	s_cmp_eq_u32 s31, 0
	s_cbranch_scc1 .LD_slow26
	global_store_dword v197, v199, s[40:41]
.LD_join27:
	ds_read_b64 v[200:201], v249 offset:0
	ds_read_b64 v[202:203], v249 offset:2048
	ds_read_b64 v[204:205], v249 offset:4096
	ds_read_b64 v[206:207], v249 offset:6144
	v_mfma_f32_32x32x16_f16 v[48:63], a[216:219], v[180:183], v[48:63]
	ds_read_b128 v[180:183], v193 offset:54272
	v_mfma_f32_32x32x16_f16 v[32:47], a[220:223], v[184:187], v[32:47]
	ds_read_b128 v[184:187], v193 offset:55296
	v_mfma_f32_32x32x16_f16 v[48:63], a[220:223], v[188:191], v[48:63]
	ds_read_b128 v[188:191], v193 offset:56320
	s_mov_b32 m0, s55
	s_add_u32 s44, s34, 0x9000
	s_addc_u32 s45, s35, 0
	global_load_lds_dwordx4 v192, s[44:45] sc1
	v_mfma_f32_32x32x16_f16 v[32:47], a[224:227], v[160:163], v[32:47]
	ds_read_b128 v[160:163], v193 offset:57344
	v_mfma_f32_32x32x16_f16 v[48:63], a[224:227], v[164:167], v[48:63]
	ds_read_b128 v[164:167], v193 offset:58368
	s_waitcnt lgkmcnt(2)
	v_mfma_f32_32x32x16_f16 v[32:47], a[228:231], v[168:171], v[32:47]
	ds_read_b128 v[168:171], v193 offset:59392
	v_mfma_f32_32x32x16_f16 v[48:63], a[228:231], v[172:175], v[48:63]
	ds_read_b128 v[172:175], v193 offset:60416
	global_load_lds_dwordx4 v192, s[44:45] offset:1024 sc1
	v_mfma_f32_32x32x16_f16 v[32:47], a[232:235], v[176:179], v[32:47]
	ds_read_b128 v[176:179], v193 offset:61440
	v_mfma_f32_32x32x16_f16 v[48:63], a[232:235], v[180:183], v[48:63]
	ds_read_b128 v[180:183], v193 offset:62464
	v_mfma_f32_32x32x16_f16 v[32:47], a[236:239], v[184:187], v[32:47]
	ds_read_b128 v[184:187], v193 offset:63488
	v_mfma_f32_32x32x16_f16 v[48:63], a[236:239], v[188:191], v[48:63]
	ds_read_b128 v[188:191], v193 offset:64512
	global_load_lds_dwordx4 v192, s[44:45] offset:2048 sc1
	s_waitcnt vmcnt(8)
	s_barrier
	s_waitcnt lgkmcnt(2)
	v_mfma_f32_32x32x16_f16 v[32:47], a[240:243], v[160:163], v[32:47]
	ds_read_b128 v[160:163], v192 offset:0
	v_add_f32_e32 v200, v200, v202
	v_add_f32_e32 v201, v201, v203
	v_add_f32_e32 v200, v200, v204
	v_add_f32_e32 v201, v201, v205
	v_add_f32_e32 v200, v200, v206
	v_add_f32_e32 v201, v201, v207
	global_store_dwordx2 v250, v[200:201], s[72:73]
	v_mfma_f32_32x32x16_f16 v[48:63], a[240:243], v[164:167], v[48:63]
	ds_read_b128 v[164:167], v192 offset:1024
	v_mfma_f32_32x32x16_f16 v[32:47], a[244:247], v[168:171], v[32:47]
	ds_read_b128 v[168:171], v192 offset:2048
	v_mfma_f32_32x32x16_f16 v[48:63], a[244:247], v[172:175], v[48:63]
	ds_read_b128 v[172:175], v192 offset:3072
	global_load_lds_dwordx4 v192, s[44:45] offset:3072 sc1
	v_mfma_f32_32x32x16_f16 v[32:47], a[248:251], v[176:179], v[32:47]
	ds_read_b128 v[176:179], v192 offset:4096
	s_and_b32 s64, s33, 1
	s_lshl_b32 s64, s64, 22
	s_add_u32 s64, s64, s50
	s_add_u32 s64, s64, 0x20000
	s_add_u32 s36, s6, s64
	s_addc_u32 s37, s7, 0
	s_lshl_b32 s64, s33, 3
	s_add_u32 s64, s64, s29
	s_lshl_b32 s64, s64, 5
	s_add_u32 s64, s64, s30
	s_lshl_b32 s64, s64, 2
	s_add_u32 s40, s8, s64
	s_addc_u32 s41, s9, 0
	s_lshl_b32 s64, s33, 19
	s_add_u32 s64, s64, 0x200
	s_add_u32 s72, s62, s64
	s_addc_u32 s73, s63, 0
	v_mfma_f32_32x32x16_f16 v[48:63], a[248:251], v[180:183], v[48:63]
	ds_read_b128 v[180:183], v192 offset:5120
	s_waitcnt lgkmcnt(2)
	v_mfma_f32_32x32x16_f16 v[32:47], a[252:255], v[184:187], v[32:47]
	ds_read_b128 v[184:187], v192 offset:6144
	v_mfma_f32_32x32x16_f16 v[48:63], a[252:255], v[188:191], v[48:63]
	ds_read_b128 v[188:191], v192 offset:7168
	s_mov_b32 m0, s56
	s_add_u32 s44, s34, 0x10000
	s_addc_u32 s45, s35, 0
	global_load_lds_dwordx4 v192, s[44:45] sc1
	s_nop 3
	s_waitcnt lgkmcnt(2)
	v_mfma_f32_32x32x16_f16 v[64:79], a[0:3], v[160:163], v[64:79]
	ds_read_b128 v[160:163], v192 offset:8192
	v_exp_f32_e32 v200, v32
	v_mfma_f32_32x32x16_f16 v[80:95], a[0:3], v[164:167], v[80:95]
	ds_read_b128 v[164:167], v192 offset:9216
	s_lshl_b32 s64, s71, 3
	s_add_u32 s64, s64, s29
	s_lshl_b32 s64, s64, 7
	s_add_u32 s38, s8, s64
	s_addc_u32 s39, s9, 0
	global_load_dword v251, v196, s[38:39] sc1
	v_exp_f32_e32 v201, v33
	v_add_f32_e32 v200, 1.0, v200
	v_mfma_f32_32x32x16_f16 v[64:79], a[4:7], v[168:171], v[64:79]
	ds_read_b128 v[168:171], v192 offset:10240
	v_exp_f32_e32 v202, v34
	v_add_f32_e32 v201, 1.0, v201
	v_mfma_f32_32x32x16_f16 v[80:95], a[4:7], v[172:175], v[80:95]
	ds_read_b128 v[172:175], v192 offset:11264
	global_load_lds_dwordx4 v192, s[44:45] offset:1024 sc1
	v_exp_f32_e32 v203, v35
	v_add_f32_e32 v202, 1.0, v202
	v_mfma_f32_32x32x16_f16 v[64:79], a[8:11], v[176:179], v[64:79]
	ds_read_b128 v[176:179], v192 offset:12288
	v_exp_f32_e32 v204, v36
	v_add_f32_e32 v203, 1.0, v203
	v_mfma_f32_32x32x16_f16 v[80:95], a[8:11], v[180:183], v[80:95]
	ds_read_b128 v[180:183], v192 offset:13312
	v_exp_f32_e32 v205, v37
	v_add_f32_e32 v204, 1.0, v204
	s_waitcnt lgkmcnt(2)
	v_mfma_f32_32x32x16_f16 v[64:79], a[12:15], v[184:187], v[64:79]
	ds_read_b128 v[184:187], v192 offset:14336
	v_exp_f32_e32 v206, v38
	v_add_f32_e32 v205, 1.0, v205
	v_mfma_f32_32x32x16_f16 v[80:95], a[12:15], v[188:191], v[80:95]
	ds_read_b128 v[188:191], v192 offset:15360
	global_load_lds_dwordx4 v192, s[44:45] offset:2048 sc1
	v_exp_f32_e32 v207, v39
	v_add_f32_e32 v206, 1.0, v206
	v_mfma_f32_32x32x16_f16 v[64:79], a[16:19], v[160:163], v[64:79]
	ds_read_b128 v[160:163], v192 offset:16384
	v_exp_f32_e32 v208, v40
	v_add_f32_e32 v207, 1.0, v207
	v_mfma_f32_32x32x16_f16 v[80:95], a[16:19], v[164:167], v[80:95]
	ds_read_b128 v[164:167], v192 offset:17408
	v_exp_f32_e32 v209, v41
	v_add_f32_e32 v208, 1.0, v208
	v_mfma_f32_32x32x16_f16 v[64:79], a[20:23], v[168:171], v[64:79]
	ds_read_b128 v[168:171], v192 offset:18432
	v_exp_f32_e32 v210, v42
	v_add_f32_e32 v209, 1.0, v209
	v_mfma_f32_32x32x16_f16 v[80:95], a[20:23], v[172:175], v[80:95]
	ds_read_b128 v[172:175], v192 offset:19456
	global_load_lds_dwordx4 v192, s[44:45] offset:3072 sc1
	v_exp_f32_e32 v211, v43
	v_add_f32_e32 v210, 1.0, v210
	s_waitcnt lgkmcnt(2)
	v_mfma_f32_32x32x16_f16 v[64:79], a[24:27], v[176:179], v[64:79]
	ds_read_b128 v[176:179], v192 offset:20480
	v_exp_f32_e32 v212, v44
	v_add_f32_e32 v211, 1.0, v211
	v_mfma_f32_32x32x16_f16 v[80:95], a[24:27], v[180:183], v[80:95]
	ds_read_b128 v[180:183], v192 offset:21504
	v_exp_f32_e32 v213, v45
	v_add_f32_e32 v212, 1.0, v212
	v_mfma_f32_32x32x16_f16 v[64:79], a[28:31], v[184:187], v[64:79]
	ds_read_b128 v[184:187], v192 offset:22528
	v_exp_f32_e32 v214, v46
	v_add_f32_e32 v213, 1.0, v213
	v_mfma_f32_32x32x16_f16 v[80:95], a[28:31], v[188:191], v[80:95]
	ds_read_b128 v[188:191], v192 offset:23552
	s_mov_b32 m0, s57
	s_add_u32 s44, s34, 0x11000
	s_addc_u32 s45, s35, 0
	global_load_lds_dwordx4 v192, s[44:45] sc1
	v_exp_f32_e32 v215, v47
	v_add_f32_e32 v214, 1.0, v214
	v_mfma_f32_32x32x16_f16 v[64:79], a[32:35], v[160:163], v[64:79]
	ds_read_b128 v[160:163], v192 offset:24576
	v_add_f32_e32 v215, 1.0, v215
	v_rcp_f32_e32 v200, v200
	v_mfma_f32_32x32x16_f16 v[80:95], a[32:35], v[164:167], v[80:95]
	ds_read_b128 v[164:167], v192 offset:25600
	v_rcp_f32_e32 v201, v201
	s_waitcnt lgkmcnt(2)
	v_mfma_f32_32x32x16_f16 v[64:79], a[36:39], v[168:171], v[64:79]
	ds_read_b128 v[168:171], v192 offset:26624
	v_rcp_f32_e32 v202, v202
	v_mfma_f32_32x32x16_f16 v[80:95], a[36:39], v[172:175], v[80:95]
	ds_read_b128 v[172:175], v192 offset:27648
	global_load_lds_dwordx4 v192, s[44:45] offset:1024 sc1
	v_rcp_f32_e32 v203, v203
	v_mfma_f32_32x32x16_f16 v[64:79], a[40:43], v[176:179], v[64:79]
	ds_read_b128 v[176:179], v192 offset:28672
	v_rcp_f32_e32 v204, v204
	v_mfma_f32_32x32x16_f16 v[80:95], a[40:43], v[180:183], v[80:95]
	ds_read_b128 v[180:183], v192 offset:29696
	v_rcp_f32_e32 v205, v205
	v_mul_f32_e32 v204, v204, v136
	v_mfma_f32_32x32x16_f16 v[64:79], a[44:47], v[184:187], v[64:79]
	ds_read_b128 v[184:187], v192 offset:30720
	v_rcp_f32_e32 v206, v206
	v_mul_f32_e32 v205, v205, v137
	v_mfma_f32_32x32x16_f16 v[80:95], a[44:47], v[188:191], v[80:95]
	ds_read_b128 v[188:191], v192 offset:31744
	global_load_lds_dwordx4 v192, s[44:45] offset:2048 sc1
	v_rcp_f32_e32 v207, v207
	v_mul_f32_e32 v206, v206, v138
	s_waitcnt vmcnt(8)
	s_barrier
	s_waitcnt lgkmcnt(2)
	v_mfma_f32_32x32x16_f16 v[64:79], a[48:51], v[160:163], v[64:79]
	ds_read_b128 v[160:163], v192 offset:32768
	v_rcp_f32_e32 v208, v208
	v_mul_f32_e32 v207, v207, v139
	v_mfma_f32_32x32x16_f16 v[80:95], a[48:51], v[164:167], v[80:95]
	ds_read_b128 v[164:167], v192 offset:33792
	v_rcp_f32_e32 v209, v209
	v_fmamk_f32 v208, v208, 0xc0b8aa3b, v198
	v_mfma_f32_32x32x16_f16 v[64:79], a[52:55], v[168:171], v[64:79]
	ds_read_b128 v[168:171], v192 offset:34816
	v_rcp_f32_e32 v210, v210
	v_fmamk_f32 v209, v209, 0xc0b8aa3b, v198
	v_fma_f32 v136, v200, v208, v204
	v_mfma_f32_32x32x16_f16 v[80:95], a[52:55], v[172:175], v[80:95]
	ds_read_b128 v[172:175], v192 offset:35840
	global_load_lds_dwordx4 v192, s[44:45] offset:3072 sc1
	v_rcp_f32_e32 v211, v211
	v_fmamk_f32 v210, v210, 0xc0b8aa3b, v198
	v_fma_f32 v137, v201, v209, v205
	v_mfma_f32_32x32x16_f16 v[64:79], a[56:59], v[176:179], v[64:79]
	ds_read_b128 v[176:179], v192 offset:36864
	v_rcp_f32_e32 v212, v212
	v_fmamk_f32 v211, v211, 0xc0b8aa3b, v198
	v_fma_f32 v138, v202, v210, v206
	v_mfma_f32_32x32x16_f16 v[80:95], a[56:59], v[180:183], v[80:95]
	ds_read_b128 v[180:183], v192 offset:37888
	v_rcp_f32_e32 v213, v213
	v_fma_f32 v139, v203, v211, v207
	s_waitcnt lgkmcnt(2)
	v_mfma_f32_32x32x16_f16 v[64:79], a[60:63], v[184:187], v[64:79]
	ds_read_b128 v[184:187], v192 offset:38912
	v_rcp_f32_e32 v214, v214
	v_mfma_f32_32x32x16_f16 v[80:95], a[60:63], v[188:191], v[80:95]
	ds_read_b128 v[188:191], v192 offset:39936
	s_mov_b32 m0, s58
	s_add_u32 s44, s34, 0x18000
	s_addc_u32 s45, s35, 0
	global_load_lds_dwordx4 v192, s[44:45] sc1
	v_rcp_f32_e32 v215, v215
	v_mfma_f32_32x32x16_f16 v[64:79], a[64:67], v[160:163], v[64:79]
	ds_read_b128 v[160:163], v192 offset:40960
	v_exp_f32_e32 v200, v136
	v_mfma_f32_32x32x16_f16 v[80:95], a[64:67], v[164:167], v[80:95]
	ds_read_b128 v[164:167], v192 offset:41984
	v_exp_f32_e32 v201, v137
	v_add_f32_e32 v200, 1.0, v200
	v_mfma_f32_32x32x16_f16 v[64:79], a[68:71], v[168:171], v[64:79]
	ds_read_b128 v[168:171], v192 offset:43008
	v_exp_f32_e32 v202, v138
	v_add_f32_e32 v201, 1.0, v201
	v_mfma_f32_32x32x16_f16 v[80:95], a[68:71], v[172:175], v[80:95]
	ds_read_b128 v[172:175], v192 offset:44032
	global_load_lds_dwordx4 v192, s[44:45] offset:1024 sc1
	v_exp_f32_e32 v203, v139
	v_add_f32_e32 v202, 1.0, v202
	s_waitcnt lgkmcnt(2)
	v_mfma_f32_32x32x16_f16 v[64:79], a[72:75], v[176:179], v[64:79]
	ds_read_b128 v[176:179], v192 offset:45056
	v_add_f32_e32 v203, 1.0, v203
	v_rcp_f32_e32 v200, v200
	v_mfma_f32_32x32x16_f16 v[80:95], a[72:75], v[180:183], v[80:95]
	ds_read_b128 v[180:183], v192 offset:46080
	v_rcp_f32_e32 v201, v201
	v_fma_f32 v200, v200, 2.0, -1.0
	v_mfma_f32_32x32x16_f16 v[64:79], a[76:79], v[184:187], v[64:79]
	ds_read_b128 v[184:187], v192 offset:47104
	v_rcp_f32_e32 v202, v202
	v_fma_f32 v201, v201, 2.0, -1.0
	v_mul_f32_e32 v216, v212, v200
	v_mfma_f32_32x32x16_f16 v[80:95], a[76:79], v[188:191], v[80:95]
	ds_read_b128 v[188:191], v192 offset:48128
	global_load_lds_dwordx4 v192, s[44:45] offset:2048 sc1
	v_rcp_f32_e32 v203, v203
	v_fma_f32 v202, v202, 2.0, -1.0
	v_mul_f32_e32 v217, v213, v201
	v_mfma_f32_32x32x16_f16 v[64:79], a[80:83], v[160:163], v[64:79]
	ds_read_b128 v[160:163], v192 offset:49152
	v_fma_f32 v203, v203, 2.0, -1.0
	v_mul_f32_e32 v218, v214, v202
	v_exp_f32_e32 v200, v48
	v_mfma_f32_32x32x16_f16 v[80:95], a[80:83], v[164:167], v[80:95]
	ds_read_b128 v[164:167], v192 offset:50176
	v_mul_f32_e32 v219, v215, v203
	v_mul_f32_e32 v236, v216, v228
	v_exp_f32_e32 v201, v49
	s_waitcnt lgkmcnt(2)
	v_mfma_f32_32x32x16_f16 v[64:79], a[84:87], v[168:171], v[64:79]
	ds_read_b128 v[168:171], v192 offset:51200
	v_mul_f32_e32 v237, v216, v232
	v_fmac_f32_e32 v236, v217, v229
	v_exp_f32_e32 v202, v50
	v_mfma_f32_32x32x16_f16 v[80:95], a[84:87], v[172:175], v[80:95]
	ds_read_b128 v[172:175], v192 offset:52224
	global_load_lds_dwordx4 v192, s[44:45] offset:3072 sc1
	v_fmac_f32_e32 v237, v217, v233
	v_fmac_f32_e32 v236, v218, v230
	v_exp_f32_e32 v203, v51
	v_mfma_f32_32x32x16_f16 v[64:79], a[88:91], v[176:179], v[64:79]
	ds_read_b128 v[176:179], v192 offset:53248
	v_fmac_f32_e32 v237, v218, v234
	v_fmac_f32_e32 v236, v219, v231
	v_exp_f32_e32 v204, v52
	v_mfma_f32_32x32x16_f16 v[80:95], a[88:91], v[180:183], v[80:95]
	ds_read_b128 v[180:183], v192 offset:54272
	v_fmac_f32_e32 v237, v219, v235
	v_mov_b32_e32 v238, v236
	v_exp_f32_e32 v205, v53
	v_mfma_f32_32x32x16_f16 v[64:79], a[92:95], v[184:187], v[64:79]
	ds_read_b128 v[184:187], v192 offset:55296
	v_mov_b32_e32 v240, v237
	v_cvt_pk_f16_f32 v220, v216, v217
	v_exp_f32_e32 v206, v54
	v_mfma_f32_32x32x16_f16 v[80:95], a[92:95], v[188:191], v[80:95]
	ds_read_b128 v[188:191], v192 offset:56320
	s_mov_b32 m0, s59
	s_add_u32 s44, s34, 0x19000
	s_addc_u32 s45, s35, 0
	global_load_lds_dwordx4 v192, s[44:45] sc1
	v_permlane32_swap_b32_e32 v236, v238
	v_permlane32_swap_b32_e32 v237, v240
	v_add_f32_e32 v238, v236, v238
	v_add_f32_e32 v239, v237, v240
	ds_write_b64 v248, v[238:239] offset:512
	v_exp_f32_e32 v207, v55
	s_waitcnt lgkmcnt(3)
	v_mfma_f32_32x32x16_f16 v[64:79], a[96:99], v[160:163], v[64:79]
	ds_read_b128 v[160:163], v192 offset:57344
	v_cvt_pk_f16_f32 v221, v218, v219
	v_exp_f32_e32 v208, v56
	v_add_f32_e32 v200, 1.0, v200
	v_mfma_f32_32x32x16_f16 v[80:95], a[96:99], v[164:167], v[80:95]
	ds_read_b128 v[164:167], v192 offset:58368
	v_exp_f32_e32 v209, v57
	v_add_f32_e32 v201, 1.0, v201
	v_add_f32_e32 v202, 1.0, v202
	v_mfma_f32_32x32x16_f16 v[64:79], a[100:103], v[168:171], v[64:79]
	ds_read_b128 v[168:171], v192 offset:59392
	v_exp_f32_e32 v210, v58
	v_add_f32_e32 v203, 1.0, v203
	v_add_f32_e32 v204, 1.0, v204
	v_mfma_f32_32x32x16_f16 v[80:95], a[100:103], v[172:175], v[80:95]
	ds_read_b128 v[172:175], v192 offset:60416
	global_load_lds_dwordx4 v192, s[44:45] offset:1024 sc1
	v_exp_f32_e32 v211, v59
	v_add_f32_e32 v205, 1.0, v205
	v_add_f32_e32 v206, 1.0, v206
	v_mfma_f32_32x32x16_f16 v[64:79], a[104:107], v[176:179], v[64:79]
	ds_read_b128 v[176:179], v192 offset:61440
	v_exp_f32_e32 v212, v60
	v_add_f32_e32 v207, 1.0, v207
	v_add_f32_e32 v208, 1.0, v208
	v_mfma_f32_32x32x16_f16 v[80:95], a[104:107], v[180:183], v[80:95]
	ds_read_b128 v[180:183], v192 offset:62464
	v_exp_f32_e32 v213, v61
	v_add_f32_e32 v209, 1.0, v209
	v_add_f32_e32 v210, 1.0, v210
	s_waitcnt lgkmcnt(2)
	v_mfma_f32_32x32x16_f16 v[64:79], a[108:111], v[184:187], v[64:79]
	ds_read_b128 v[184:187], v192 offset:63488
	v_exp_f32_e32 v214, v62
	v_add_f32_e32 v211, 1.0, v211
	v_add_f32_e32 v212, 1.0, v212
	v_mfma_f32_32x32x16_f16 v[80:95], a[108:111], v[188:191], v[80:95]
	ds_read_b128 v[188:191], v192 offset:64512
	global_load_lds_dwordx4 v192, s[44:45] offset:2048 sc1
	v_exp_f32_e32 v215, v63
	v_add_f32_e32 v213, 1.0, v213
	v_add_f32_e32 v214, 1.0, v214
	s_waitcnt vmcnt(7)
	s_barrier
	v_mfma_f32_32x32x16_f16 v[64:79], a[112:115], v[160:163], v[64:79]
	ds_read_b128 v[160:163], v193 offset:0
	v_add_f32_e32 v215, 1.0, v215
	v_rcp_f32_e32 v200, v200
	v_mfma_f32_32x32x16_f16 v[80:95], a[112:115], v[164:167], v[80:95]
	ds_read_b128 v[164:167], v193 offset:1024
	v_rcp_f32_e32 v201, v201
	v_mfma_f32_32x32x16_f16 v[64:79], a[116:119], v[168:171], v[64:79]
	ds_read_b128 v[168:171], v193 offset:2048
	v_rcp_f32_e32 v202, v202
	v_mfma_f32_32x32x16_f16 v[80:95], a[116:119], v[172:175], v[80:95]
	ds_read_b128 v[172:175], v193 offset:3072
	global_load_lds_dwordx4 v192, s[44:45] offset:3072 sc1
	v_rcp_f32_e32 v203, v203
	s_waitcnt lgkmcnt(2)
	v_mfma_f32_32x32x16_f16 v[64:79], a[120:123], v[176:179], v[64:79]
	ds_read_b128 v[176:179], v193 offset:4096
	v_rcp_f32_e32 v204, v204
	s_add_u32 s46, s42, 0x0
	s_addc_u32 s47, s43, 0
	global_load_dwordx4 v[0:3], v192, s[46:47] offset:0
	v_mfma_f32_32x32x16_f16 v[80:95], a[120:123], v[180:183], v[80:95]
	ds_read_b128 v[180:183], v193 offset:5120
	v_rcp_f32_e32 v205, v205
	v_mul_f32_e32 v204, v204, v140
	global_load_dwordx4 v[4:7], v192, s[46:47] offset:1024
	global_load_dwordx4 v[8:11], v192, s[46:47] offset:2048
	v_mfma_f32_32x32x16_f16 v[64:79], a[124:127], v[184:187], v[64:79]
	ds_read_b128 v[184:187], v193 offset:6144
	v_rcp_f32_e32 v206, v206
	v_mul_f32_e32 v205, v205, v141
	global_load_dwordx4 v[12:15], v192, s[46:47] offset:3072
	s_add_u32 s46, s42, 0x1000
	s_addc_u32 s47, s43, 0
	v_mfma_f32_32x32x16_f16 v[80:95], a[124:127], v[188:191], v[80:95]
	ds_read_b128 v[188:191], v193 offset:7168
	v_cmp_gt_u32_e32 vcc, 4, v251
	s_cbranch_vccnz .LD_tpoll29

.LD_join31:
	s_waitcnt lgkmcnt(3)
	v_mfma_f32_32x32x16_f16 v[64:79], a[180:183], v[168:171], v[64:79]
	ds_read_b128 v[168:171], v193 offset:34816
	v_mfma_f32_32x32x16_f16 v[80:95], a[180:183], v[172:175], v[80:95]
	ds_read_b128 v[172:175], v193 offset:35840
	global_load_lds_dwordx4 v192, s[44:45] offset:3072 sc1
	v_mfma_f32_32x32x16_f16 v[64:79], a[184:187], v[176:179], v[64:79]
	ds_read_b128 v[176:179], v193 offset:36864
	v_mfma_f32_32x32x16_f16 v[80:95], a[184:187], v[180:183], v[80:95]
	ds_read_b128 v[180:183], v193 offset:37888
	v_mfma_f32_32x32x16_f16 v[64:79], a[188:191], v[184:187], v[64:79]
	ds_read_b128 v[184:187], v193 offset:38912
	v_mfma_f32_32x32x16_f16 v[80:95], a[188:191], v[188:191], v[80:95]
	ds_read_b128 v[188:191], v193 offset:39936
	s_mov_b32 m0, s54
	s_add_u32 s44, s34, 0x8000
	s_addc_u32 s45, s35, 0
	global_load_lds_dwordx4 v192, s[44:45] sc1
	s_waitcnt lgkmcnt(2)
	v_mfma_f32_32x32x16_f16 v[64:79], a[192:195], v[160:163], v[64:79]
	ds_read_b128 v[160:163], v193 offset:40960
	v_mfma_f32_32x32x16_f16 v[80:95], a[192:195], v[164:167], v[80:95]
	ds_read_b128 v[164:167], v193 offset:41984
	v_mfma_f32_32x32x16_f16 v[64:79], a[196:199], v[168:171], v[64:79]
	ds_read_b128 v[168:171], v193 offset:43008
	v_mfma_f32_32x32x16_f16 v[80:95], a[196:199], v[172:175], v[80:95]
	ds_read_b128 v[172:175], v193 offset:44032
	global_load_lds_dwordx4 v192, s[44:45] offset:1024 sc1
	v_mfma_f32_32x32x16_f16 v[64:79], a[200:203], v[176:179], v[64:79]
	ds_read_b128 v[176:179], v193 offset:45056
	v_mfma_f32_32x32x16_f16 v[80:95], a[200:203], v[180:183], v[80:95]
	ds_read_b128 v[180:183], v193 offset:46080
	s_waitcnt lgkmcnt(2)
	v_mfma_f32_32x32x16_f16 v[64:79], a[204:207], v[184:187], v[64:79]
	ds_read_b128 v[184:187], v193 offset:47104
	v_mfma_f32_32x32x16_f16 v[80:95], a[204:207], v[188:191], v[80:95]
	ds_read_b128 v[188:191], v193 offset:48128
	global_load_lds_dwordx4 v192, s[44:45] offset:2048 sc1
	v_mfma_f32_32x32x16_f16 v[64:79], a[208:211], v[160:163], v[64:79]
	ds_read_b128 v[160:163], v193 offset:49152
	v_mfma_f32_32x32x16_f16 v[80:95], a[208:211], v[164:167], v[80:95]
	ds_read_b128 v[164:167], v193 offset:50176
	v_mfma_f32_32x32x16_f16 v[64:79], a[212:215], v[168:171], v[64:79]
	ds_read_b128 v[168:171], v193 offset:51200
	v_mfma_f32_32x32x16_f16 v[80:95], a[212:215], v[172:175], v[80:95]
	ds_read_b128 v[172:175], v193 offset:52224
	global_load_lds_dwordx4 v192, s[44:45] offset:3072 sc1
	s_waitcnt lgkmcnt(2)
	v_mfma_f32_32x32x16_f16 v[64:79], a[216:219], v[176:179], v[64:79]
	ds_read_b128 v[176:179], v193 offset:53248
	s_waitcnt vmcnt(5)
	s_barrier
	v_mov_b32_e32 v199, 2
	s_cmp_eq_u32 s31, 0
	s_cbranch_scc1 .LD_slow32
	global_store_dword v197, v199, s[40:41]
.LD_join33:
	ds_read_b64 v[200:201], v249 offset:512
	ds_read_b64 v[202:203], v249 offset:2560
	ds_read_b64 v[204:205], v249 offset:4608
	ds_read_b64 v[206:207], v249 offset:6656
	v_mfma_f32_32x32x16_f16 v[80:95], a[216:219], v[180:183], v[80:95]
	ds_read_b128 v[180:183], v193 offset:54272
	v_mfma_f32_32x32x16_f16 v[64:79], a[220:223], v[184:187], v[64:79]
	ds_read_b128 v[184:187], v193 offset:55296
	v_mfma_f32_32x32x16_f16 v[80:95], a[220:223], v[188:191], v[80:95]
	ds_read_b128 v[188:191], v193 offset:56320
	s_mov_b32 m0, s55
	s_add_u32 s44, s34, 0x9000
	s_addc_u32 s45, s35, 0
	global_load_lds_dwordx4 v192, s[44:45] sc1
	v_mfma_f32_32x32x16_f16 v[64:79], a[224:227], v[160:163], v[64:79]
	ds_read_b128 v[160:163], v193 offset:57344
	v_mfma_f32_32x32x16_f16 v[80:95], a[224:227], v[164:167], v[80:95]
	ds_read_b128 v[164:167], v193 offset:58368
	s_waitcnt lgkmcnt(2)
	v_mfma_f32_32x32x16_f16 v[64:79], a[228:231], v[168:171], v[64:79]
	ds_read_b128 v[168:171], v193 offset:59392
	v_mfma_f32_32x32x16_f16 v[80:95], a[228:231], v[172:175], v[80:95]
	ds_read_b128 v[172:175], v193 offset:60416
	global_load_lds_dwordx4 v192, s[44:45] offset:1024 sc1
	v_mfma_f32_32x32x16_f16 v[64:79], a[232:235], v[176:179], v[64:79]
	ds_read_b128 v[176:179], v193 offset:61440
	v_mfma_f32_32x32x16_f16 v[80:95], a[232:235], v[180:183], v[80:95]
	ds_read_b128 v[180:183], v193 offset:62464
	v_mfma_f32_32x32x16_f16 v[64:79], a[236:239], v[184:187], v[64:79]
	ds_read_b128 v[184:187], v193 offset:63488
	v_mfma_f32_32x32x16_f16 v[80:95], a[236:239], v[188:191], v[80:95]
	ds_read_b128 v[188:191], v193 offset:64512
	global_load_lds_dwordx4 v192, s[44:45] offset:2048 sc1
	s_waitcnt vmcnt(8)
	s_barrier
	s_waitcnt lgkmcnt(2)
	v_mfma_f32_32x32x16_f16 v[64:79], a[240:243], v[160:163], v[64:79]
	ds_read_b128 v[160:163], v192 offset:0
	v_add_f32_e32 v200, v200, v202
	v_add_f32_e32 v201, v201, v203
	v_add_f32_e32 v200, v200, v204
	v_add_f32_e32 v201, v201, v205
	v_add_f32_e32 v200, v200, v206
	v_add_f32_e32 v201, v201, v207
	global_store_dwordx2 v250, v[200:201], s[72:73]
	v_mfma_f32_32x32x16_f16 v[80:95], a[240:243], v[164:167], v[80:95]
	ds_read_b128 v[164:167], v192 offset:1024
	v_mfma_f32_32x32x16_f16 v[64:79], a[244:247], v[168:171], v[64:79]
	ds_read_b128 v[168:171], v192 offset:2048
	v_mfma_f32_32x32x16_f16 v[80:95], a[244:247], v[172:175], v[80:95]
	ds_read_b128 v[172:175], v192 offset:3072
	global_load_lds_dwordx4 v192, s[44:45] offset:3072 sc1
	v_mfma_f32_32x32x16_f16 v[64:79], a[248:251], v[176:179], v[64:79]
	ds_read_b128 v[176:179], v192 offset:4096
	s_and_b32 s64, s33, 1
	s_lshl_b32 s64, s64, 22
	s_add_u32 s64, s64, s50
	s_add_u32 s64, s64, 0x40000
	s_add_u32 s36, s6, s64
	s_addc_u32 s37, s7, 0
	s_lshl_b32 s64, s33, 3
	s_add_u32 s64, s64, s29
	s_lshl_b32 s64, s64, 5
	s_add_u32 s64, s64, s30
	s_lshl_b32 s64, s64, 2
	s_add_u32 s40, s8, s64
	s_addc_u32 s41, s9, 0
	s_lshl_b32 s64, s33, 19
	s_add_u32 s64, s64, 0x400
	s_add_u32 s72, s62, s64
	s_addc_u32 s73, s63, 0
	v_mfma_f32_32x32x16_f16 v[80:95], a[248:251], v[180:183], v[80:95]
	ds_read_b128 v[180:183], v192 offset:5120
	s_waitcnt lgkmcnt(2)
	v_mfma_f32_32x32x16_f16 v[64:79], a[252:255], v[184:187], v[64:79]
	ds_read_b128 v[184:187], v192 offset:6144
	v_mfma_f32_32x32x16_f16 v[80:95], a[252:255], v[188:191], v[80:95]
	ds_read_b128 v[188:191], v192 offset:7168
	s_mov_b32 m0, s56
	s_add_u32 s44, s34, 0x10000
	s_addc_u32 s45, s35, 0
	global_load_lds_dwordx4 v192, s[44:45] sc1
	s_nop 3
	s_waitcnt lgkmcnt(2)
	v_mfma_f32_32x32x16_f16 v[96:111], a[0:3], v[160:163], v[96:111]
	ds_read_b128 v[160:163], v192 offset:8192
	v_exp_f32_e32 v200, v64
	v_mfma_f32_32x32x16_f16 v[112:127], a[0:3], v[164:167], v[112:127]
	ds_read_b128 v[164:167], v192 offset:9216
	s_lshl_b32 s64, s33, 3
	s_add_u32 s64, s64, s29
	s_lshl_b32 s64, s64, 7
	s_add_u32 s38, s8, s64
	s_addc_u32 s39, s9, 0
	global_load_dword v251, v196, s[38:39] sc1
	v_exp_f32_e32 v201, v65
	v_add_f32_e32 v200, 1.0, v200
	v_mfma_f32_32x32x16_f16 v[96:111], a[4:7], v[168:171], v[96:111]
	ds_read_b128 v[168:171], v192 offset:10240
	v_exp_f32_e32 v202, v66
	v_add_f32_e32 v201, 1.0, v201
	v_mfma_f32_32x32x16_f16 v[112:127], a[4:7], v[172:175], v[112:127]
	ds_read_b128 v[172:175], v192 offset:11264
	global_load_lds_dwordx4 v192, s[44:45] offset:1024 sc1
	v_exp_f32_e32 v203, v67
	v_add_f32_e32 v202, 1.0, v202
	v_mfma_f32_32x32x16_f16 v[96:111], a[8:11], v[176:179], v[96:111]
	ds_read_b128 v[176:179], v192 offset:12288
	v_exp_f32_e32 v204, v68
	v_add_f32_e32 v203, 1.0, v203
	v_mfma_f32_32x32x16_f16 v[112:127], a[8:11], v[180:183], v[112:127]
	ds_read_b128 v[180:183], v192 offset:13312
	v_exp_f32_e32 v205, v69
	v_add_f32_e32 v204, 1.0, v204
	s_waitcnt lgkmcnt(2)
	v_mfma_f32_32x32x16_f16 v[96:111], a[12:15], v[184:187], v[96:111]
	ds_read_b128 v[184:187], v192 offset:14336
	v_exp_f32_e32 v206, v70
	v_add_f32_e32 v205, 1.0, v205
	v_mfma_f32_32x32x16_f16 v[112:127], a[12:15], v[188:191], v[112:127]
	ds_read_b128 v[188:191], v192 offset:15360
	global_load_lds_dwordx4 v192, s[44:45] offset:2048 sc1
	v_exp_f32_e32 v207, v71
	v_add_f32_e32 v206, 1.0, v206
	v_mfma_f32_32x32x16_f16 v[96:111], a[16:19], v[160:163], v[96:111]
	ds_read_b128 v[160:163], v192 offset:16384
	v_exp_f32_e32 v208, v72
	v_add_f32_e32 v207, 1.0, v207
	v_mfma_f32_32x32x16_f16 v[112:127], a[16:19], v[164:167], v[112:127]
	ds_read_b128 v[164:167], v192 offset:17408
	v_exp_f32_e32 v209, v73
	v_add_f32_e32 v208, 1.0, v208
	v_mfma_f32_32x32x16_f16 v[96:111], a[20:23], v[168:171], v[96:111]
	ds_read_b128 v[168:171], v192 offset:18432
	v_exp_f32_e32 v210, v74
	v_add_f32_e32 v209, 1.0, v209
	v_mfma_f32_32x32x16_f16 v[112:127], a[20:23], v[172:175], v[112:127]
	ds_read_b128 v[172:175], v192 offset:19456
	global_load_lds_dwordx4 v192, s[44:45] offset:3072 sc1
	v_exp_f32_e32 v211, v75
	v_add_f32_e32 v210, 1.0, v210
	s_waitcnt lgkmcnt(2)
	v_mfma_f32_32x32x16_f16 v[96:111], a[24:27], v[176:179], v[96:111]
	ds_read_b128 v[176:179], v192 offset:20480
	v_exp_f32_e32 v212, v76
	v_add_f32_e32 v211, 1.0, v211
	v_mfma_f32_32x32x16_f16 v[112:127], a[24:27], v[180:183], v[112:127]
	ds_read_b128 v[180:183], v192 offset:21504
	v_exp_f32_e32 v213, v77
	v_add_f32_e32 v212, 1.0, v212
	v_mfma_f32_32x32x16_f16 v[96:111], a[28:31], v[184:187], v[96:111]
	ds_read_b128 v[184:187], v192 offset:22528
	v_exp_f32_e32 v214, v78
	v_add_f32_e32 v213, 1.0, v213
	v_mfma_f32_32x32x16_f16 v[112:127], a[28:31], v[188:191], v[112:127]
	ds_read_b128 v[188:191], v192 offset:23552
	s_mov_b32 m0, s57
	s_add_u32 s44, s34, 0x11000
	s_addc_u32 s45, s35, 0
	global_load_lds_dwordx4 v192, s[44:45] sc1
	v_exp_f32_e32 v215, v79
	v_add_f32_e32 v214, 1.0, v214
	v_mfma_f32_32x32x16_f16 v[96:111], a[32:35], v[160:163], v[96:111]
	ds_read_b128 v[160:163], v192 offset:24576
	v_add_f32_e32 v215, 1.0, v215
	v_rcp_f32_e32 v200, v200
	v_mfma_f32_32x32x16_f16 v[112:127], a[32:35], v[164:167], v[112:127]
	ds_read_b128 v[164:167], v192 offset:25600
	v_rcp_f32_e32 v201, v201
	s_waitcnt lgkmcnt(2)
	v_mfma_f32_32x32x16_f16 v[96:111], a[36:39], v[168:171], v[96:111]
	ds_read_b128 v[168:171], v192 offset:26624
	v_rcp_f32_e32 v202, v202
	v_mfma_f32_32x32x16_f16 v[112:127], a[36:39], v[172:175], v[112:127]
	ds_read_b128 v[172:175], v192 offset:27648
	global_load_lds_dwordx4 v192, s[44:45] offset:1024 sc1
	v_rcp_f32_e32 v203, v203
	v_mfma_f32_32x32x16_f16 v[96:111], a[40:43], v[176:179], v[96:111]
	ds_read_b128 v[176:179], v192 offset:28672
	v_rcp_f32_e32 v204, v204
	v_mfma_f32_32x32x16_f16 v[112:127], a[40:43], v[180:183], v[112:127]
	ds_read_b128 v[180:183], v192 offset:29696
	v_rcp_f32_e32 v205, v205
	v_mul_f32_e32 v204, v204, v144
	v_mfma_f32_32x32x16_f16 v[96:111], a[44:47], v[184:187], v[96:111]
	ds_read_b128 v[184:187], v192 offset:30720
	v_rcp_f32_e32 v206, v206
	v_mul_f32_e32 v205, v205, v145
	v_mfma_f32_32x32x16_f16 v[112:127], a[44:47], v[188:191], v[112:127]
	ds_read_b128 v[188:191], v192 offset:31744
	global_load_lds_dwordx4 v192, s[44:45] offset:2048 sc1
	v_rcp_f32_e32 v207, v207
	v_mul_f32_e32 v206, v206, v146
	s_waitcnt vmcnt(8)
	s_barrier
	s_waitcnt lgkmcnt(2)
	v_mfma_f32_32x32x16_f16 v[96:111], a[48:51], v[160:163], v[96:111]
	ds_read_b128 v[160:163], v192 offset:32768
	v_rcp_f32_e32 v208, v208
	v_mul_f32_e32 v207, v207, v147
	v_mfma_f32_32x32x16_f16 v[112:127], a[48:51], v[164:167], v[112:127]
	ds_read_b128 v[164:167], v192 offset:33792
	v_rcp_f32_e32 v209, v209
	v_fmamk_f32 v208, v208, 0xc0b8aa3b, v198
	v_mfma_f32_32x32x16_f16 v[96:111], a[52:55], v[168:171], v[96:111]
	ds_read_b128 v[168:171], v192 offset:34816
	v_rcp_f32_e32 v210, v210
	v_fmamk_f32 v209, v209, 0xc0b8aa3b, v198
	v_fma_f32 v144, v200, v208, v204
	v_mfma_f32_32x32x16_f16 v[112:127], a[52:55], v[172:175], v[112:127]
	ds_read_b128 v[172:175], v192 offset:35840
	global_load_lds_dwordx4 v192, s[44:45] offset:3072 sc1
	v_rcp_f32_e32 v211, v211
	v_fmamk_f32 v210, v210, 0xc0b8aa3b, v198
	v_fma_f32 v145, v201, v209, v205
	v_mfma_f32_32x32x16_f16 v[96:111], a[56:59], v[176:179], v[96:111]
	ds_read_b128 v[176:179], v192 offset:36864
	v_rcp_f32_e32 v212, v212
	v_fmamk_f32 v211, v211, 0xc0b8aa3b, v198
	v_fma_f32 v146, v202, v210, v206
	v_mfma_f32_32x32x16_f16 v[112:127], a[56:59], v[180:183], v[112:127]
	ds_read_b128 v[180:183], v192 offset:37888
	v_rcp_f32_e32 v213, v213
	v_fma_f32 v147, v203, v211, v207
	s_waitcnt lgkmcnt(2)
	v_mfma_f32_32x32x16_f16 v[96:111], a[60:63], v[184:187], v[96:111]
	ds_read_b128 v[184:187], v192 offset:38912
	v_rcp_f32_e32 v214, v214
	v_mfma_f32_32x32x16_f16 v[112:127], a[60:63], v[188:191], v[112:127]
	ds_read_b128 v[188:191], v192 offset:39936
	s_mov_b32 m0, s58
	s_add_u32 s44, s34, 0x18000
	s_addc_u32 s45, s35, 0
	global_load_lds_dwordx4 v192, s[44:45] sc1
	v_rcp_f32_e32 v215, v215
	v_mfma_f32_32x32x16_f16 v[96:111], a[64:67], v[160:163], v[96:111]
	ds_read_b128 v[160:163], v192 offset:40960
	v_exp_f32_e32 v200, v144
	v_mfma_f32_32x32x16_f16 v[112:127], a[64:67], v[164:167], v[112:127]
	ds_read_b128 v[164:167], v192 offset:41984
	v_exp_f32_e32 v201, v145
	v_add_f32_e32 v200, 1.0, v200
	v_mfma_f32_32x32x16_f16 v[96:111], a[68:71], v[168:171], v[96:111]
	ds_read_b128 v[168:171], v192 offset:43008
	v_exp_f32_e32 v202, v146
	v_add_f32_e32 v201, 1.0, v201
	v_mfma_f32_32x32x16_f16 v[112:127], a[68:71], v[172:175], v[112:127]
	ds_read_b128 v[172:175], v192 offset:44032
	global_load_lds_dwordx4 v192, s[44:45] offset:1024 sc1
	v_exp_f32_e32 v203, v147
	v_add_f32_e32 v202, 1.0, v202
	s_waitcnt lgkmcnt(2)
	v_mfma_f32_32x32x16_f16 v[96:111], a[72:75], v[176:179], v[96:111]
	ds_read_b128 v[176:179], v192 offset:45056
	v_add_f32_e32 v203, 1.0, v203
	v_rcp_f32_e32 v200, v200
	v_mfma_f32_32x32x16_f16 v[112:127], a[72:75], v[180:183], v[112:127]
	ds_read_b128 v[180:183], v192 offset:46080
	v_rcp_f32_e32 v201, v201
	v_fma_f32 v200, v200, 2.0, -1.0
	v_mfma_f32_32x32x16_f16 v[96:111], a[76:79], v[184:187], v[96:111]
	ds_read_b128 v[184:187], v192 offset:47104
	v_rcp_f32_e32 v202, v202
	v_fma_f32 v201, v201, 2.0, -1.0
	v_mul_f32_e32 v216, v212, v200
	v_mfma_f32_32x32x16_f16 v[112:127], a[76:79], v[188:191], v[112:127]
	ds_read_b128 v[188:191], v192 offset:48128
	global_load_lds_dwordx4 v192, s[44:45] offset:2048 sc1
	v_rcp_f32_e32 v203, v203
	v_fma_f32 v202, v202, 2.0, -1.0
	v_mul_f32_e32 v217, v213, v201
	v_mfma_f32_32x32x16_f16 v[96:111], a[80:83], v[160:163], v[96:111]
	ds_read_b128 v[160:163], v192 offset:49152
	v_fma_f32 v203, v203, 2.0, -1.0
	v_mul_f32_e32 v218, v214, v202
	v_exp_f32_e32 v200, v80
	v_mfma_f32_32x32x16_f16 v[112:127], a[80:83], v[164:167], v[112:127]
	ds_read_b128 v[164:167], v192 offset:50176
	v_mul_f32_e32 v219, v215, v203
	v_mul_f32_e32 v236, v216, v228
	v_exp_f32_e32 v201, v81
	s_waitcnt lgkmcnt(2)
	v_mfma_f32_32x32x16_f16 v[96:111], a[84:87], v[168:171], v[96:111]
	ds_read_b128 v[168:171], v192 offset:51200
	v_mul_f32_e32 v237, v216, v232
	v_fmac_f32_e32 v236, v217, v229
	v_exp_f32_e32 v202, v82
	v_mfma_f32_32x32x16_f16 v[112:127], a[84:87], v[172:175], v[112:127]
	ds_read_b128 v[172:175], v192 offset:52224
	global_load_lds_dwordx4 v192, s[44:45] offset:3072 sc1
	v_fmac_f32_e32 v237, v217, v233
	v_fmac_f32_e32 v236, v218, v230
	v_exp_f32_e32 v203, v83
	v_mfma_f32_32x32x16_f16 v[96:111], a[88:91], v[176:179], v[96:111]
	ds_read_b128 v[176:179], v192 offset:53248
	v_fmac_f32_e32 v237, v218, v234
	v_fmac_f32_e32 v236, v219, v231
	v_exp_f32_e32 v204, v84
	v_mfma_f32_32x32x16_f16 v[112:127], a[88:91], v[180:183], v[112:127]
	ds_read_b128 v[180:183], v192 offset:54272
	v_fmac_f32_e32 v237, v219, v235
	v_mov_b32_e32 v238, v236
	v_exp_f32_e32 v205, v85
	v_mfma_f32_32x32x16_f16 v[96:111], a[92:95], v[184:187], v[96:111]
	ds_read_b128 v[184:187], v192 offset:55296
	v_mov_b32_e32 v240, v237
	v_cvt_pk_f16_f32 v220, v216, v217
	v_exp_f32_e32 v206, v86
	v_mfma_f32_32x32x16_f16 v[112:127], a[92:95], v[188:191], v[112:127]
	ds_read_b128 v[188:191], v192 offset:56320
	s_mov_b32 m0, s59
	s_add_u32 s44, s34, 0x19000
	s_addc_u32 s45, s35, 0
	global_load_lds_dwordx4 v192, s[44:45] sc1
	v_permlane32_swap_b32_e32 v236, v238
	v_permlane32_swap_b32_e32 v237, v240
	v_add_f32_e32 v238, v236, v238
	v_add_f32_e32 v239, v237, v240
	ds_write_b64 v248, v[238:239] offset:1024
	v_exp_f32_e32 v207, v87
	s_waitcnt lgkmcnt(3)
	v_mfma_f32_32x32x16_f16 v[96:111], a[96:99], v[160:163], v[96:111]
	ds_read_b128 v[160:163], v192 offset:57344
	v_cvt_pk_f16_f32 v221, v218, v219
	v_exp_f32_e32 v208, v88
	v_add_f32_e32 v200, 1.0, v200
	v_mfma_f32_32x32x16_f16 v[112:127], a[96:99], v[164:167], v[112:127]
	ds_read_b128 v[164:167], v192 offset:58368
	v_exp_f32_e32 v209, v89
	v_add_f32_e32 v201, 1.0, v201
	v_add_f32_e32 v202, 1.0, v202
	v_mfma_f32_32x32x16_f16 v[96:111], a[100:103], v[168:171], v[96:111]
	ds_read_b128 v[168:171], v192 offset:59392
	v_exp_f32_e32 v210, v90
	v_add_f32_e32 v203, 1.0, v203
	v_add_f32_e32 v204, 1.0, v204
	v_mfma_f32_32x32x16_f16 v[112:127], a[100:103], v[172:175], v[112:127]
	ds_read_b128 v[172:175], v192 offset:60416
	global_load_lds_dwordx4 v192, s[44:45] offset:1024 sc1
	v_exp_f32_e32 v211, v91
	v_add_f32_e32 v205, 1.0, v205
	v_add_f32_e32 v206, 1.0, v206
	v_mfma_f32_32x32x16_f16 v[96:111], a[104:107], v[176:179], v[96:111]
	ds_read_b128 v[176:179], v192 offset:61440
	v_exp_f32_e32 v212, v92
	v_add_f32_e32 v207, 1.0, v207
	v_add_f32_e32 v208, 1.0, v208
	v_mfma_f32_32x32x16_f16 v[112:127], a[104:107], v[180:183], v[112:127]
	ds_read_b128 v[180:183], v192 offset:62464
	v_exp_f32_e32 v213, v93
	v_add_f32_e32 v209, 1.0, v209
	v_add_f32_e32 v210, 1.0, v210
	s_waitcnt lgkmcnt(2)
	v_mfma_f32_32x32x16_f16 v[96:111], a[108:111], v[184:187], v[96:111]
	ds_read_b128 v[184:187], v192 offset:63488
	v_exp_f32_e32 v214, v94
	v_add_f32_e32 v211, 1.0, v211
	v_add_f32_e32 v212, 1.0, v212
	v_mfma_f32_32x32x16_f16 v[112:127], a[108:111], v[188:191], v[112:127]
	ds_read_b128 v[188:191], v192 offset:64512
	global_load_lds_dwordx4 v192, s[44:45] offset:2048 sc1
	v_exp_f32_e32 v215, v95
	v_add_f32_e32 v213, 1.0, v213
	v_add_f32_e32 v214, 1.0, v214
	s_waitcnt vmcnt(7)
	s_barrier
	v_mfma_f32_32x32x16_f16 v[96:111], a[112:115], v[160:163], v[96:111]
	ds_read_b128 v[160:163], v193 offset:0
	v_add_f32_e32 v215, 1.0, v215
	v_rcp_f32_e32 v200, v200
	v_mfma_f32_32x32x16_f16 v[112:127], a[112:115], v[164:167], v[112:127]
	ds_read_b128 v[164:167], v193 offset:1024
	v_rcp_f32_e32 v201, v201
	v_mfma_f32_32x32x16_f16 v[96:111], a[116:119], v[168:171], v[96:111]
	ds_read_b128 v[168:171], v193 offset:2048
	v_rcp_f32_e32 v202, v202
	v_mfma_f32_32x32x16_f16 v[112:127], a[116:119], v[172:175], v[112:127]
	ds_read_b128 v[172:175], v193 offset:3072
	global_load_lds_dwordx4 v192, s[44:45] offset:3072 sc1
	v_rcp_f32_e32 v203, v203
	s_waitcnt lgkmcnt(2)
	v_mfma_f32_32x32x16_f16 v[96:111], a[120:123], v[176:179], v[96:111]
	ds_read_b128 v[176:179], v193 offset:4096
	v_rcp_f32_e32 v204, v204
	s_add_u32 s46, s42, 0x2000
	s_addc_u32 s47, s43, 0
	global_load_dwordx4 v[32:35], v192, s[46:47] offset:0
	v_mfma_f32_32x32x16_f16 v[112:127], a[120:123], v[180:183], v[112:127]
	ds_read_b128 v[180:183], v193 offset:5120
	v_rcp_f32_e32 v205, v205
	v_mul_f32_e32 v204, v204, v148
	global_load_dwordx4 v[36:39], v192, s[46:47] offset:1024
	global_load_dwordx4 v[40:43], v192, s[46:47] offset:2048
	v_mfma_f32_32x32x16_f16 v[96:111], a[124:127], v[184:187], v[96:111]
	ds_read_b128 v[184:187], v193 offset:6144
	v_rcp_f32_e32 v206, v206
	v_mul_f32_e32 v205, v205, v149
	global_load_dwordx4 v[44:47], v192, s[46:47] offset:3072
	s_add_u32 s46, s42, 0x3000
	s_addc_u32 s47, s43, 0
	v_mfma_f32_32x32x16_f16 v[112:127], a[124:127], v[188:191], v[112:127]
	ds_read_b128 v[188:191], v193 offset:7168
	v_cmp_gt_u32_e32 vcc, 1, v251
	s_cbranch_vccnz .LD_tpoll35

.LD_join37:
	s_waitcnt lgkmcnt(3)
	v_mfma_f32_32x32x16_f16 v[96:111], a[180:183], v[168:171], v[96:111]
	ds_read_b128 v[168:171], v193 offset:34816
	v_mfma_f32_32x32x16_f16 v[112:127], a[180:183], v[172:175], v[112:127]
	ds_read_b128 v[172:175], v193 offset:35840
	global_load_lds_dwordx4 v192, s[44:45] offset:3072 sc1
	v_mfma_f32_32x32x16_f16 v[96:111], a[184:187], v[176:179], v[96:111]
	ds_read_b128 v[176:179], v193 offset:36864
	v_mfma_f32_32x32x16_f16 v[112:127], a[184:187], v[180:183], v[112:127]
	ds_read_b128 v[180:183], v193 offset:37888
	v_mfma_f32_32x32x16_f16 v[96:111], a[188:191], v[184:187], v[96:111]
	ds_read_b128 v[184:187], v193 offset:38912
	v_mfma_f32_32x32x16_f16 v[112:127], a[188:191], v[188:191], v[112:127]
	ds_read_b128 v[188:191], v193 offset:39936
	s_mov_b32 m0, s54
	s_add_u32 s44, s34, 0x8000
	s_addc_u32 s45, s35, 0
	global_load_lds_dwordx4 v192, s[44:45] sc1
	s_waitcnt lgkmcnt(2)
	v_mfma_f32_32x32x16_f16 v[96:111], a[192:195], v[160:163], v[96:111]
	ds_read_b128 v[160:163], v193 offset:40960
	v_mfma_f32_32x32x16_f16 v[112:127], a[192:195], v[164:167], v[112:127]
	ds_read_b128 v[164:167], v193 offset:41984
	v_mfma_f32_32x32x16_f16 v[96:111], a[196:199], v[168:171], v[96:111]
	ds_read_b128 v[168:171], v193 offset:43008
	v_mfma_f32_32x32x16_f16 v[112:127], a[196:199], v[172:175], v[112:127]
	ds_read_b128 v[172:175], v193 offset:44032
	global_load_lds_dwordx4 v192, s[44:45] offset:1024 sc1
	v_mfma_f32_32x32x16_f16 v[96:111], a[200:203], v[176:179], v[96:111]
	ds_read_b128 v[176:179], v193 offset:45056
	v_mfma_f32_32x32x16_f16 v[112:127], a[200:203], v[180:183], v[112:127]
	ds_read_b128 v[180:183], v193 offset:46080
	s_waitcnt lgkmcnt(2)
	v_mfma_f32_32x32x16_f16 v[96:111], a[204:207], v[184:187], v[96:111]
	ds_read_b128 v[184:187], v193 offset:47104
	v_mfma_f32_32x32x16_f16 v[112:127], a[204:207], v[188:191], v[112:127]
	ds_read_b128 v[188:191], v193 offset:48128
	global_load_lds_dwordx4 v192, s[44:45] offset:2048 sc1
	v_mfma_f32_32x32x16_f16 v[96:111], a[208:211], v[160:163], v[96:111]
	ds_read_b128 v[160:163], v193 offset:49152
	v_mfma_f32_32x32x16_f16 v[112:127], a[208:211], v[164:167], v[112:127]
	ds_read_b128 v[164:167], v193 offset:50176
	v_mfma_f32_32x32x16_f16 v[96:111], a[212:215], v[168:171], v[96:111]
	ds_read_b128 v[168:171], v193 offset:51200
	v_mfma_f32_32x32x16_f16 v[112:127], a[212:215], v[172:175], v[112:127]
	ds_read_b128 v[172:175], v193 offset:52224
	global_load_lds_dwordx4 v192, s[44:45] offset:3072 sc1
	s_waitcnt lgkmcnt(2)
	v_mfma_f32_32x32x16_f16 v[96:111], a[216:219], v[176:179], v[96:111]
	ds_read_b128 v[176:179], v193 offset:53248
	s_waitcnt vmcnt(5)
	s_barrier
	v_mov_b32_e32 v199, 3
	s_cmp_eq_u32 s31, 0
	s_cbranch_scc1 .LD_slow38
	global_store_dword v197, v199, s[40:41]
.LD_join39:
	ds_read_b64 v[200:201], v249 offset:1024
	ds_read_b64 v[202:203], v249 offset:3072
	ds_read_b64 v[204:205], v249 offset:5120
	ds_read_b64 v[206:207], v249 offset:7168
	v_mfma_f32_32x32x16_f16 v[112:127], a[216:219], v[180:183], v[112:127]
	ds_read_b128 v[180:183], v193 offset:54272
	v_mfma_f32_32x32x16_f16 v[96:111], a[220:223], v[184:187], v[96:111]
	ds_read_b128 v[184:187], v193 offset:55296
	v_mfma_f32_32x32x16_f16 v[112:127], a[220:223], v[188:191], v[112:127]
	ds_read_b128 v[188:191], v193 offset:56320
	s_mov_b32 m0, s55
	s_add_u32 s44, s34, 0x9000
	s_addc_u32 s45, s35, 0
	global_load_lds_dwordx4 v192, s[44:45] sc1
	v_mfma_f32_32x32x16_f16 v[96:111], a[224:227], v[160:163], v[96:111]
	ds_read_b128 v[160:163], v193 offset:57344
	v_mfma_f32_32x32x16_f16 v[112:127], a[224:227], v[164:167], v[112:127]
	ds_read_b128 v[164:167], v193 offset:58368
	s_waitcnt lgkmcnt(2)
	v_mfma_f32_32x32x16_f16 v[96:111], a[228:231], v[168:171], v[96:111]
	ds_read_b128 v[168:171], v193 offset:59392
	v_mfma_f32_32x32x16_f16 v[112:127], a[228:231], v[172:175], v[112:127]
	ds_read_b128 v[172:175], v193 offset:60416
	global_load_lds_dwordx4 v192, s[44:45] offset:1024 sc1
	v_mfma_f32_32x32x16_f16 v[96:111], a[232:235], v[176:179], v[96:111]
	ds_read_b128 v[176:179], v193 offset:61440
	v_mfma_f32_32x32x16_f16 v[112:127], a[232:235], v[180:183], v[112:127]
	ds_read_b128 v[180:183], v193 offset:62464
	v_mfma_f32_32x32x16_f16 v[96:111], a[236:239], v[184:187], v[96:111]
	ds_read_b128 v[184:187], v193 offset:63488
	v_mfma_f32_32x32x16_f16 v[112:127], a[236:239], v[188:191], v[112:127]
	ds_read_b128 v[188:191], v193 offset:64512
	global_load_lds_dwordx4 v192, s[44:45] offset:2048 sc1
	s_waitcnt vmcnt(8)
	s_barrier
	s_waitcnt lgkmcnt(2)
	v_mfma_f32_32x32x16_f16 v[96:111], a[240:243], v[160:163], v[96:111]
	ds_read_b128 v[160:163], v192 offset:0
	v_add_f32_e32 v200, v200, v202
	v_add_f32_e32 v201, v201, v203
	v_add_f32_e32 v200, v200, v204
	v_add_f32_e32 v201, v201, v205
	v_add_f32_e32 v200, v200, v206
	v_add_f32_e32 v201, v201, v207
	global_store_dwordx2 v250, v[200:201], s[72:73]
	v_mfma_f32_32x32x16_f16 v[112:127], a[240:243], v[164:167], v[112:127]
	ds_read_b128 v[164:167], v192 offset:1024
	v_mfma_f32_32x32x16_f16 v[96:111], a[244:247], v[168:171], v[96:111]
	ds_read_b128 v[168:171], v192 offset:2048
	v_mfma_f32_32x32x16_f16 v[112:127], a[244:247], v[172:175], v[112:127]
	ds_read_b128 v[172:175], v192 offset:3072
	global_load_lds_dwordx4 v192, s[44:45] offset:3072 sc1
	v_mfma_f32_32x32x16_f16 v[96:111], a[248:251], v[176:179], v[96:111]
	ds_read_b128 v[176:179], v192 offset:4096
	v_mfma_f32_32x32x16_f16 v[112:127], a[248:251], v[180:183], v[112:127]
	ds_read_b128 v[180:183], v192 offset:5120
	s_waitcnt lgkmcnt(2)
	v_mfma_f32_32x32x16_f16 v[96:111], a[252:255], v[184:187], v[96:111]
	ds_read_b128 v[184:187], v192 offset:6144
	v_mfma_f32_32x32x16_f16 v[112:127], a[252:255], v[188:191], v[112:127]
	ds_read_b128 v[188:191], v192 offset:7168
	s_mov_b32 m0, s56
	s_add_u32 s44, s34, 0x10000
	s_addc_u32 s45, s35, 0
	global_load_lds_dwordx4 v192, s[44:45] sc1
	s_add_u32 s33, s33, 1
	s_cmp_lt_u32 s33, s28
	s_cbranch_scc1 .LD_loop12
